# attention main loop: half-step stagger of waves 4-7 vs 0-3 (barrier at QK/PV boundary for waves 4-7), V tile DMA shifted one tile later, SGPR-pointer LDS-DMA blocks
# baseline (speedup 1.0000x reference)
; __device__ __forceinline__ void attn_unit(const unsigned char* __restrict__ CQt, const unsigned char* __restrict__ Wh, const f32x2* __restrict__ cst, const unsigned char* __restrict__ Kh, const unsigned char* __restrict__ Vh, bf16* __restrict__ Ob, char* lds) {
;     ...
;       if (s3 == 2) {
; #pragma unroll
;         for (int r = 0; r < 16; r += 2) { const f32x2 c0 = cc[r >> 1], c1 = cc[8 + (r >> 1)];
;           const float x0 = a0[r], y0 = a0[r + 1], x1 = a1[r], y1 = a1[r + 1];
;           a0[r] = x0 * c0.x - y0 * c0.y; a0[r + 1] = y0 * c0.x + x0 * c0.y; a1[r] = x1 * c1.x - y1 * c1.y; a1[r + 1] = y1 * c1.x + x1 * c1.y; } }
; #pragma unroll
;       for (int q = 0; q < 4; ++q) { int u0 = 0, u1 = 0;
;         u0 = __builtin_amdgcn_cvt_pk_fp8_f32(a0[4 * q] * QS, a0[4 * q + 1] * QS, u0, false); u0 = __builtin_amdgcn_cvt_pk_fp8_f32(a0[4 * q + 2] * QS, a0[4 * q + 3] * QS, u0, true);
;         u1 = __builtin_amdgcn_cvt_pk_fp8_f32(a1[4 * q] * QS, a1[4 * q + 1] * QS, u1, false); u1 = __builtin_amdgcn_cvt_pk_fp8_f32(a1[4 * q + 2] * QS, a1[4 * q + 3] * QS, u1, true);
;         qr[s3][q] = u0; qr[s3][4 + q] = u1; }
.LBB0_886:
	v_mul_f32_e32 v2, 0x3c553b94, v2
	v_mul_f32_e32 v3, 0x3c553b94, v3
	v_mov_b32_e32 v142, 0
	v_cvt_pk_fp8_f32 v142, v2, v3
	v_mul_f32_e32 v2, 0x3c553b94, v4
	v_mul_f32_e32 v3, 0x3c553b94, v5
	v_mov_b32_e32 v139, 0
	v_cvt_pk_fp8_f32 v142, v2, v3 op_sel:[0,0,1]
	v_mul_f32_e32 v2, 0x3c553b94, v22
	v_mul_f32_e32 v3, 0x3c553b94, v23
	v_cvt_pk_fp8_f32 v139, v2, v3
	v_mul_f32_e32 v4, 0x3c553b94, v6
	v_mul_f32_e32 v5, 0x3c553b94, v7
	v_mov_b32_e32 v143, 0
	v_cvt_pk_fp8_f32 v143, v4, v5
	v_mul_f32_e32 v2, 0x3c553b94, v24
	v_mul_f32_e32 v3, 0x3c553b94, v25
	v_cvt_pk_fp8_f32 v139, v2, v3 op_sel:[0,0,1]
	v_mul_f32_e32 v2, 0x3c553b94, v8
	v_mul_f32_e32 v3, 0x3c553b94, v9
	v_cvt_pk_fp8_f32 v143, v2, v3 op_sel:[0,0,1]
	v_mul_f32_e32 v2, 0x3c553b94, v26
	v_mul_f32_e32 v3, 0x3c553b94, v27
	v_mov_b32_e32 v140, 0
	v_cvt_pk_fp8_f32 v140, v2, v3
	v_mul_f32_e32 v4, 0x3c553b94, v10
	v_mul_f32_e32 v5, 0x3c553b94, v11
	v_mov_b32_e32 v144, 0
	v_cvt_pk_fp8_f32 v144, v4, v5
	v_mul_f32_e32 v2, 0x3c553b94, v28
	v_mul_f32_e32 v3, 0x3c553b94, v29
	v_cvt_pk_fp8_f32 v140, v2, v3 op_sel:[0,0,1]
	v_mul_f32_e32 v2, 0x3c553b94, v12
	v_mul_f32_e32 v3, 0x3c553b94, v13
	v_cvt_pk_fp8_f32 v144, v2, v3 op_sel:[0,0,1]
	v_mul_f32_e32 v2, 0x3c553b94, v30
	v_mul_f32_e32 v3, 0x3c553b94, v31
	v_mov_b32_e32 v141, 0
	v_cvt_pk_fp8_f32 v141, v2, v3
	v_mul_f32_e32 v4, 0x3c553b94, v14
	v_mul_f32_e32 v5, 0x3c553b94, v15
	v_mov_b32_e32 v145, 0
	v_cvt_pk_fp8_f32 v145, v4, v5
	v_mul_f32_e32 v2, 0x3c553b94, v32
	v_mul_f32_e32 v3, 0x3c553b94, v33
	v_cvt_pk_fp8_f32 v141, v2, v3 op_sel:[0,0,1]
	v_mul_f32_e32 v2, 0x3c553b94, v16
	v_mul_f32_e32 v3, 0x3c553b94, v17
	v_cvt_pk_fp8_f32 v145, v2, v3 op_sel:[0,0,1]
	v_mul_f32_e32 v2, 0x3c553b94, v50
	v_mul_f32_e32 v3, 0x3c553b94, v51
	v_mov_b32_e32 v146, 0
	v_cvt_pk_fp8_f32 v146, v2, v3
	v_mul_f32_e32 v4, 0x3c553b94, v34
	v_mul_f32_e32 v5, 0x3c553b94, v35
	v_mov_b32_e32 v150, 0
	v_cvt_pk_fp8_f32 v150, v4, v5
	v_mul_f32_e32 v2, 0x3c553b94, v52
	v_mul_f32_e32 v3, 0x3c553b94, v53
	v_cvt_pk_fp8_f32 v146, v2, v3 op_sel:[0,0,1]
	v_mul_f32_e32 v2, 0x3c553b94, v36
	v_mul_f32_e32 v3, 0x3c553b94, v37
	v_cvt_pk_fp8_f32 v150, v2, v3 op_sel:[0,0,1]
	v_mul_f32_e32 v2, 0x3c553b94, v54
	v_mul_f32_e32 v3, 0x3c553b94, v55
	v_mov_b32_e32 v147, 0
	v_cvt_pk_fp8_f32 v147, v2, v3
	v_mul_f32_e32 v4, 0x3c553b94, v38
	v_mul_f32_e32 v5, 0x3c553b94, v39
	v_mov_b32_e32 v151, 0
	v_cvt_pk_fp8_f32 v151, v4, v5
	v_mul_f32_e32 v2, 0x3c553b94, v56
	v_mul_f32_e32 v3, 0x3c553b94, v57
	v_cvt_pk_fp8_f32 v147, v2, v3 op_sel:[0,0,1]
	v_mul_f32_e32 v2, 0x3c553b94, v40
	v_mul_f32_e32 v3, 0x3c553b94, v41
	v_cvt_pk_fp8_f32 v151, v2, v3 op_sel:[0,0,1]
	v_mul_f32_e32 v2, 0x3c553b94, v58
	v_mul_f32_e32 v3, 0x3c553b94, v59
	v_mov_b32_e32 v148, 0
	v_cvt_pk_fp8_f32 v148, v2, v3
	v_mul_f32_e32 v4, 0x3c553b94, v42
	v_mul_f32_e32 v5, 0x3c553b94, v43
	v_mov_b32_e32 v152, 0
	v_cvt_pk_fp8_f32 v152, v4, v5
	v_mul_f32_e32 v2, 0x3c553b94, v60
	v_mul_f32_e32 v3, 0x3c553b94, v61
	v_cvt_pk_fp8_f32 v148, v2, v3 op_sel:[0,0,1]
	v_mul_f32_e32 v2, 0x3c553b94, v44
	v_mul_f32_e32 v3, 0x3c553b94, v45
	v_cvt_pk_fp8_f32 v152, v2, v3 op_sel:[0,0,1]
	v_mul_f32_e32 v2, 0x3c553b94, v62
	v_mul_f32_e32 v3, 0x3c553b94, v63
	v_mov_b32_e32 v149, 0
	v_cvt_pk_fp8_f32 v149, v2, v3
	v_mul_f32_e32 v4, 0x3c553b94, v46
	v_mul_f32_e32 v5, 0x3c553b94, v47
	v_mov_b32_e32 v153, 0
	v_cvt_pk_fp8_f32 v153, v4, v5
	v_mul_f32_e32 v2, 0x3c553b94, v64
	v_mul_f32_e32 v3, 0x3c553b94, v65
	v_cvt_pk_fp8_f32 v149, v2, v3 op_sel:[0,0,1]
	v_mul_f32_e32 v2, 0x3c553b94, v48
	v_mul_f32_e32 v3, 0x3c553b94, v49
	v_cvt_pk_fp8_f32 v153, v2, v3 op_sel:[0,0,1]
	s_waitcnt vmcnt(0)
	v_pk_mul_f32 v[2:3], v[134:135], v[82:83]
	v_mov_b32_e32 v154, 0
	v_sub_f32_e32 v4, v2, v3
	v_pk_mul_f32 v[2:3], v[134:135], v[82:83] op_sel:[0,1] op_sel_hi:[1,0]
	v_mov_b32_e32 v158, 0
	v_add_f32_e32 v5, v2, v3
	v_pk_mul_f32 v[2:3], v[136:137], v[84:85]
	s_mov_b32 m0, s88
	v_sub_f32_e32 v10, v2, v3
	v_pk_mul_f32 v[2:3], v[136:137], v[84:85] op_sel:[0,1] op_sel_hi:[1,0]
	v_or_b32_e32 v99, 1, v156
	v_add_f32_e32 v11, v2, v3
	v_pk_mul_f32 v[2:3], v[130:131], v[86:87]
	v_lshrrev_b32_e32 v65, 2, v189
	v_sub_f32_e32 v34, v2, v3
	v_pk_mul_f32 v[2:3], v[130:131], v[86:87] op_sel:[0,1] op_sel_hi:[1,0]
	v_mul_u32_u24_e32 v64, 0xc0, v170
	v_add_f32_e32 v35, v2, v3
	v_pk_mul_f32 v[2:3], v[132:133], v[88:89]
	v_mul_f32_e32 v18, 0x3c553b94, v18
	v_sub_f32_e32 v36, v2, v3
	v_pk_mul_f32 v[2:3], v[132:133], v[88:89] op_sel:[0,1] op_sel_hi:[1,0]
	v_mul_f32_e32 v19, 0x3c553b94, v19
	v_add_f32_e32 v37, v2, v3
	v_pk_mul_f32 v[2:3], v[126:127], v[90:91]
	v_mov_b32_e32 v138, 0
	v_sub_f32_e32 v50, v2, v3
	v_pk_mul_f32 v[2:3], v[126:127], v[90:91] op_sel:[0,1] op_sel_hi:[1,0]
	v_cvt_pk_fp8_f32 v138, v18, v19
	v_add_f32_e32 v51, v2, v3
	v_pk_mul_f32 v[2:3], v[128:129], v[92:93]
	v_mul_f32_e32 v18, 0x3c553b94, v20
	v_sub_f32_e32 v52, v2, v3
	v_pk_mul_f32 v[2:3], v[128:129], v[92:93] op_sel:[0,1] op_sel_hi:[1,0]
	v_mul_f32_e32 v19, 0x3c553b94, v21
	v_add_f32_e32 v53, v2, v3
	v_pk_mul_f32 v[2:3], v[122:123], v[94:95]
	v_cvt_pk_fp8_f32 v138, v18, v19 op_sel:[0,0,1]
	v_sub_f32_e32 v54, v2, v3
	v_pk_mul_f32 v[2:3], v[122:123], v[94:95] op_sel:[0,1] op_sel_hi:[1,0]
	v_mov_b32_e32 v155, 0
	v_add_f32_e32 v55, v2, v3
	v_pk_mul_f32 v[2:3], v[124:125], v[96:97]
	v_mov_b32_e32 v159, 0
	v_sub_f32_e32 v56, v2, v3
	v_pk_mul_f32 v[2:3], v[124:125], v[96:97] op_sel:[0,1] op_sel_hi:[1,0]
	v_or_b32_e32 v100, 4, v156
	v_add_f32_e32 v57, v2, v3
	v_pk_mul_f32 v[2:3], v[118:119], v[66:67]
	v_or_b32_e32 v101, 5, v156
	v_sub_f32_e32 v6, v2, v3
	v_pk_mul_f32 v[2:3], v[118:119], v[66:67] op_sel:[0,1] op_sel_hi:[1,0]
; __device__ __forceinline__ void qkt(f32x16& p0, f32x16& p1, const char* Ks, const v8i* qr, int r32, int hi, const f32x16& nm16) {
; #pragma unroll
;   for (int s = 0; s < 3; ++s) { const int c0 = 4 * s + 2 * hi;
;     const v8i a0 = __builtin_shufflevector(*reinterpret_cast<const v4i*>(Ks + k8_off(r32, c0)), *reinterpret_cast<const v4i*>(Ks + k8_off(r32, c0 + 1)), 0, 1, 2, 3, 4, 5, 6, 7);
;     const v8i a1 = __builtin_shufflevector(*reinterpret_cast<const v4i*>(Ks + 32 * DQK + k8_off(r32, c0)), *reinterpret_cast<const v4i*>(Ks + 32 * DQK + k8_off(r32, c0 + 1)), 0, 1, 2, 3, 4, 5, 6, 7);
;     p0 = __builtin_amdgcn_mfma_scale_f32_32x32x64_f8f6f4(a0, qr[s], s == 0 ? nm16 : p0, 0, 0, 0, 0, 0, 0);
;     p1 = __builtin_amdgcn_mfma_scale_f32_32x32x64_f8f6f4(a1, qr[s], s == 0 ? nm16 : p1, 0, 0, 0, 0, 0, 0); }
; }
; __device__ __forceinline__ void attn_unit(const unsigned char* __restrict__ CQt, const unsigned char* __restrict__ Wh, const f32x2* __restrict__ cst, const unsigned char* __restrict__ Kh, const unsigned char* __restrict__ Vh, bf16* __restrict__ Ob, char* lds) {
;     ...
;       if (s3 == 2) {
; #pragma unroll
;         for (int r = 0; r < 16; r += 2) { const f32x2 c0 = cc[r >> 1], c1 = cc[8 + (r >> 1)];
;           const float x0 = a0[r], y0 = a0[r + 1], x1 = a1[r], y1 = a1[r + 1];
;           a0[r] = x0 * c0.x - y0 * c0.y; a0[r + 1] = y0 * c0.x + x0 * c0.y; a1[r] = x1 * c1.x - y1 * c1.y; a1[r + 1] = y1 * c1.x + x1 * c1.y; } }
; #pragma unroll
;       for (int q = 0; q < 4; ++q) { int u0 = 0, u1 = 0;
;         u0 = __builtin_amdgcn_cvt_pk_fp8_f32(a0[4 * q] * QS, a0[4 * q + 1] * QS, u0, false); u0 = __builtin_amdgcn_cvt_pk_fp8_f32(a0[4 * q + 2] * QS, a0[4 * q + 3] * QS, u0, true);
;         u1 = __builtin_amdgcn_cvt_pk_fp8_f32(a1[4 * q] * QS, a1[4 * q + 1] * QS, u1, false); u1 = __builtin_amdgcn_cvt_pk_fp8_f32(a1[4 * q + 2] * QS, a1[4 * q + 3] * QS, u1, true);
;         qr[s3][q] = u0; qr[s3][4 + q] = u1; }
;     }
;     asm volatile("s_waitcnt lgkmcnt(0)" ::: "memory"); __builtin_amdgcn_s_barrier(); asm volatile("" ::: "memory");
;   }
;   ADMA(1, 1);
;   qkt(pA0, pA1, lds + KS(0), qr, r32, hi, nm16); partialSM<true>(pA0, pA1, m_reg, nm16, alA);
	v_mul_f32_e32 v6, 0x3c553b94, v6
	v_add_f32_e32 v7, v2, v3
	v_pk_mul_f32 v[2:3], v[120:121], v[68:69]
	v_mul_f32_e32 v7, 0x3c553b94, v7
	v_sub_f32_e32 v8, v2, v3
	v_pk_mul_f32 v[2:3], v[120:121], v[68:69] op_sel:[0,1] op_sel_hi:[1,0]
	v_cvt_pk_fp8_f32 v154, v6, v7
	v_add_f32_e32 v9, v2, v3
	v_pk_mul_f32 v[2:3], v[114:115], v[70:71]
	v_bitop3_b32 v6, v99, v65, 3 bitop3:0x78
	v_sub_f32_e32 v12, v2, v3
	v_pk_mul_f32 v[2:3], v[114:115], v[70:71] op_sel:[0,1] op_sel_hi:[1,0]
	v_lshlrev_b32_e32 v203, 4, v6
	v_add_f32_e32 v13, v2, v3
	v_pk_mul_f32 v[2:3], v[116:117], v[72:73]
	v_or_b32_e32 v6, v203, v64
	v_sub_f32_e32 v38, v2, v3
	v_pk_mul_f32 v[2:3], v[116:117], v[72:73] op_sel:[0,1] op_sel_hi:[1,0]
	v_add_u32_e32 v197, 0, v6
	v_add_f32_e32 v39, v2, v3
	v_pk_mul_f32 v[2:3], v[110:111], v[74:75]
	v_mul_f32_e32 v42, 0x3c553b94, v12
	v_sub_f32_e32 v40, v2, v3
	v_pk_mul_f32 v[2:3], v[110:111], v[74:75] op_sel:[0,1] op_sel_hi:[1,0]
	v_mul_f32_e32 v43, 0x3c553b94, v13
	v_add_f32_e32 v41, v2, v3
	v_pk_mul_f32 v[2:3], v[112:113], v[76:77]
	v_cvt_pk_fp8_f32 v155, v42, v43
	v_sub_f32_e32 v58, v2, v3
	v_pk_mul_f32 v[2:3], v[112:113], v[76:77] op_sel:[0,1] op_sel_hi:[1,0]
	v_or_b32_e32 v102, 8, v156
	v_add_f32_e32 v59, v2, v3
	v_pk_mul_f32 v[2:3], v[106:107], v[78:79]
	v_or_b32_e32 v103, 9, v156
	v_sub_f32_e32 v60, v2, v3
	v_pk_mul_f32 v[2:3], v[106:107], v[78:79] op_sel:[0,1] op_sel_hi:[1,0]
	v_mul_f32_e32 v10, 0x3c553b94, v10
	v_add_f32_e32 v61, v2, v3
	v_pk_mul_f32 v[2:3], v[108:109], v[80:81]
	v_mul_f32_e32 v11, 0x3c553b94, v11
	v_sub_f32_e32 v62, v2, v3
	v_pk_mul_f32 v[2:3], v[108:109], v[80:81] op_sel:[0,1] op_sel_hi:[1,0]
	v_mul_f32_e32 v50, 0x3c553b94, v50
	v_add_f32_e32 v63, v2, v3
	v_mul_f32_e32 v2, 0x3c553b94, v8
	v_mul_f32_e32 v3, 0x3c553b94, v9
	v_cvt_pk_fp8_f32 v154, v2, v3 op_sel:[0,0,1]
	v_mul_f32_e32 v2, 0x3c553b94, v4
	v_mul_f32_e32 v3, 0x3c553b94, v5
	v_cvt_pk_fp8_f32 v158, v2, v3
	v_lshl_add_u64 v[2:3], v[168:169], 0, 64
	global_load_lds_dwordx4 v[2:3], off
	v_bitop3_b32 v2, v156, v65, 3 bitop3:0x78
	v_lshlrev_b32_e32 v202, 4, v2
	v_or_b32_e32 v2, v202, v64
	v_add_u32_e32 v196, 0, v2
	ds_read_b128 v[2:5], v196 offset:8192
	ds_read_b128 v[6:9], v197 offset:8192
	s_waitcnt lgkmcnt(0)
	v_mfma_f32_32x32x64_f8f6f4 v[18:33], v[2:9], v[138:145], 0
	v_mul_f32_e32 v4, 0x3c553b94, v34
	v_mul_f32_e32 v5, 0x3c553b94, v35
	v_cvt_pk_fp8_f32 v159, v4, v5
	v_mul_f32_e32 v2, 0x3c553b94, v38
	v_mul_f32_e32 v3, 0x3c553b94, v39
	v_cvt_pk_fp8_f32 v155, v2, v3 op_sel:[0,0,1]
	v_mul_f32_e32 v2, 0x3c553b94, v36
	v_mul_f32_e32 v3, 0x3c553b94, v37
	v_cvt_pk_fp8_f32 v159, v2, v3 op_sel:[0,0,1]
	v_mul_f32_e32 v2, 0x3c553b94, v40
	v_mul_f32_e32 v3, 0x3c553b94, v41
	v_mov_b32_e32 v156, 0
	v_cvt_pk_fp8_f32 v156, v2, v3
	v_bitop3_b32 v2, v100, v65, 3 bitop3:0x78
	v_bitop3_b32 v6, v101, v65, 3 bitop3:0x78
	v_lshl_add_u32 v2, v2, 4, v64
	v_lshl_add_u32 v6, v6, 4, v64
	v_cvt_pk_fp8_f32 v158, v10, v11 op_sel:[0,0,1]
	ds_read_b128 v[10:13], v196 offset:14336
	ds_read_b128 v[14:17], v197 offset:14336
	v_add_u32_e32 v198, 0, v2
	v_add_u32_e32 v199, 0, v6
	ds_read_b128 v[2:5], v198 offset:8192
	ds_read_b128 v[6:9], v199 offset:8192
	s_waitcnt lgkmcnt(0)
	v_mfma_f32_32x32x64_f8f6f4 v[34:49], v[10:17], v[138:145], 0
	v_mul_f32_e32 v51, 0x3c553b94, v51
	v_mov_b32_e32 v160, 0
	v_cvt_pk_fp8_f32 v160, v50, v51
	v_mov_b32_e32 v157, 0
	v_mul_f32_e32 v10, 0x3c553b94, v58
	v_mul_f32_e32 v11, 0x3c553b94, v59
	v_mov_b32_e32 v161, 0
	v_cvt_pk_fp8_f32 v156, v10, v11 op_sel:[0,0,1]
	ds_read_b128 v[10:13], v198 offset:14336
	ds_read_b128 v[14:17], v199 offset:14336
	s_mov_b32 s9, s8
	s_mov_b32 s10, s8
	s_mov_b32 s11, s8
	s_mov_b32 s12, s8
	s_mov_b32 s13, s8
	s_mov_b32 s14, s8
	v_mfma_f32_32x32x64_f8f6f4 v[18:33], v[2:9], v[146:153], v[18:33]
	v_mul_f32_e32 v4, 0x3c553b94, v60
	v_mul_f32_e32 v5, 0x3c553b94, v61
	v_cvt_pk_fp8_f32 v157, v4, v5
	v_mul_f32_e32 v2, 0x3c553b94, v52
	v_mul_f32_e32 v3, 0x3c553b94, v53
	v_cvt_pk_fp8_f32 v160, v2, v3 op_sel:[0,0,1]
	v_mul_f32_e32 v2, 0x3c553b94, v62
	v_mul_f32_e32 v3, 0x3c553b94, v63
	v_cvt_pk_fp8_f32 v157, v2, v3 op_sel:[0,0,1]
	v_mul_f32_e32 v2, 0x3c553b94, v54
	v_mul_f32_e32 v3, 0x3c553b94, v55
	v_cvt_pk_fp8_f32 v161, v2, v3
	v_bitop3_b32 v2, v102, v65, 3 bitop3:0x78
	v_bitop3_b32 v6, v103, v65, 3 bitop3:0x78
	v_lshl_add_u32 v2, v2, 4, v64
	v_lshl_add_u32 v6, v6, 4, v64
	v_add_u32_e32 v200, 0, v2
	v_add_u32_e32 v201, 0, v6
	ds_read_b128 v[2:5], v200 offset:8192
	ds_read_b128 v[6:9], v201 offset:8192
	s_waitcnt lgkmcnt(0)
	v_mfma_f32_32x32x64_f8f6f4 v[34:49], v[10:17], v[146:153], v[34:49]
	v_mul_f32_e32 v10, 0x3c553b94, v56
	v_mul_f32_e32 v11, 0x3c553b94, v57
	v_cvt_pk_fp8_f32 v161, v10, v11 op_sel:[0,0,1]
	ds_read_b128 v[50:53], v200 offset:14336
	ds_read_b128 v[54:57], v201 offset:14336
	s_mov_b32 s15, s8
	s_mov_b32 s16, s8
	s_mov_b32 s17, s8
	s_mov_b32 s18, s8
	s_mov_b32 s19, s8
	s_mov_b32 s20, s8
	s_mov_b32 s21, s8
	s_mov_b32 s22, s8
	s_mov_b32 s23, s8
	v_mov_b32_e32 v66, 0
	v_mov_b32_e32 v67, 0
	v_mfma_f32_32x32x64_f8f6f4 v[18:33], v[2:9], v[154:161], v[18:33]
	v_mov_b64_e32 v[2:3], s[8:9]
	v_mov_b64_e32 v[4:5], s[10:11]
	v_mov_b64_e32 v[6:7], s[12:13]
	v_mov_b64_e32 v[8:9], s[14:15]
	v_mov_b64_e32 v[10:11], s[16:17]
	v_mov_b64_e32 v[12:13], s[18:19]
	v_mov_b64_e32 v[14:15], s[20:21]
	v_mov_b64_e32 v[16:17], s[22:23]
	s_lshl_b32 s9, s33, 10
	s_and_b32 s9, s9, 0xffff0000
	v_mov_b32_e32 v68, 0
	v_mov_b32_e32 v69, 0
	v_mov_b32_e32 v70, 0
	v_mov_b32_e32 v71, 0
	v_mov_b32_e32 v72, 0
	s_waitcnt lgkmcnt(0)
; template <bool FIRST>
; __device__ __forceinline__ void partialSM(f32x16& p0, f32x16& p1, float& m_reg, f32x16& nm16, float& alpha) {
;   float pmax = p0[0];
; #pragma unroll
;   for (int r = 1; r < 16; ++r) pmax = fmaxf(pmax, p0[r]);
; #pragma unroll
;   for (int r = 0; r < 16; ++r) pmax = fmaxf(pmax, p1[r]);
;   { auto rr = __builtin_amdgcn_permlane32_swap(__float_as_uint(pmax), __float_as_uint(pmax), false, false);
;     pmax = fmaxf(__uint_as_float(rr[0]), __uint_as_float(rr[1])); }
;   if (!FIRST && __builtin_expect(__all(pmax <= THR2), 1)) { alpha = 1.f; }
;   else { const float d = FIRST ? pmax : fmaxf(pmax, 0.f);
;     alpha = FIRST ? 1.f : __builtin_amdgcn_exp2f(-d); m_reg += d;
;     const float nm = -m_reg;
; #pragma unroll
;     for (int r = 0; r < 16; ++r) { p0[r] -= d; p1[r] -= d; float t = nm16[r]; asm volatile("v_mov_b32 %0, %1" : "+v"(t) : "v"(nm)); nm16[r] = t; } }
; #pragma unroll
;   for (int r = 0; r < 16; ++r) p0[r] = __builtin_amdgcn_exp2f(p0[r]);
; }
	v_mfma_f32_32x32x64_f8f6f4 v[34:49], v[50:57], v[154:161], v[34:49]
	s_nop 2
	v_max_f32_e32 v50, v19, v19
	v_max_f32_e32 v51, v18, v18
	v_max_f32_e32 v50, v51, v50
	v_max3_f32 v50, v50, v20, v21
	v_max3_f32 v50, v50, v22, v23
	v_max3_f32 v50, v50, v24, v25
	v_max3_f32 v50, v50, v26, v27
	v_max3_f32 v50, v50, v28, v29
	v_max3_f32 v50, v50, v30, v31
	v_max3_f32 v50, v50, v32, v33
	v_mov_b32_e32 v73, 0
	v_mov_b32_e32 v74, 0
	v_mov_b32_e32 v75, 0
	v_mov_b32_e32 v76, 0
	v_mov_b32_e32 v77, 0
	s_nop 1
	v_max3_f32 v50, v50, v34, v35
	v_max3_f32 v50, v50, v36, v37
	v_max3_f32 v50, v50, v38, v39
	v_max3_f32 v50, v50, v40, v41
	v_max3_f32 v50, v50, v42, v43
	v_max3_f32 v50, v50, v44, v45
	v_max3_f32 v50, v50, v46, v47
	v_max3_f32 v50, v50, v48, v49
	v_mov_b32_e32 v51, v50
	s_nop 1
	v_permlane32_swap_b32_e32 v50, v51
	v_max_f32_e32 v51, v51, v51
	v_max_f32_e32 v50, v50, v50
	v_max_f32_e32 v50, v50, v51
	v_sub_f32_e32 v18, v18, v50
	v_add_f32_e32 v195, 0, v50
	v_sub_f32_e32 v19, v19, v50
	v_sub_f32_e32 v20, v20, v50
	v_sub_f32_e32 v21, v21, v50
	v_sub_f32_e32 v22, v22, v50
	v_sub_f32_e32 v23, v23, v50
	v_sub_f32_e32 v24, v24, v50
	v_sub_f32_e32 v25, v25, v50
	v_sub_f32_e32 v26, v26, v50
	v_sub_f32_e32 v27, v27, v50
	v_sub_f32_e32 v28, v28, v50
	v_sub_f32_e32 v29, v29, v50
	v_sub_f32_e32 v30, v30, v50
	v_mov_b32_e32 v78, 0
	v_sub_f32_e32 v31, v31, v50
	v_mov_b32_e32 v79, 0
	v_sub_f32_e32 v32, v32, v50
	v_mov_b32_e32 v80, 0
	v_sub_f32_e32 v33, v33, v50
	v_mov_b32_e32 v81, 0
	v_exp_f32_e32 v235, v18
	v_lshl_or_b32 v18, v171, 10, s9
	s_lshl_b32 s2, s2, 2
	v_xor_b32_e32 v51, 0x80000000, v195
	v_mov_b32 v66, v51
	v_mov_b32 v67, v51
	v_mov_b32 v68, v51
	v_mov_b32 v69, v51
	v_mov_b32 v70, v51
	v_mov_b32 v71, v51
	v_mov_b32 v72, v51
	v_mov_b32 v73, v51
	v_mov_b32 v74, v51
	v_mov_b32 v75, v51
	v_mov_b32 v76, v51
	v_mov_b32 v77, v51
	v_mov_b32 v78, v51
	v_mov_b32 v79, v51
	v_mov_b32 v80, v51
	v_mov_b32 v81, v51
	v_exp_f32_e32 v236, v19
	v_exp_f32_e32 v233, v20
	v_exp_f32_e32 v234, v21
	v_exp_f32_e32 v231, v22
	v_exp_f32_e32 v232, v23
	v_exp_f32_e32 v229, v24
	v_exp_f32_e32 v230, v25
	v_exp_f32_e32 v227, v26
	v_exp_f32_e32 v228, v27
	v_exp_f32_e32 v225, v28
	v_exp_f32_e32 v226, v29
	v_exp_f32_e32 v223, v30
	v_exp_f32_e32 v224, v31
	v_exp_f32_e32 v221, v32
	v_exp_f32_e32 v222, v33
	s_waitcnt vmcnt(0)
	v_and_or_b32 v18, v18, s84, v172
	s_add_i32 s93, s2, 0
	s_barrier
	v_ashrrev_i32_e32 v19, 31, v18
	v_lshlrev_b32_e32 v98, 4, v190
	v_mov_b32_e32 v162, 0
	v_sub_f32_e32 v97, v49, v50
	v_sub_f32_e32 v96, v48, v50
	v_sub_f32_e32 v95, v47, v50
	v_sub_f32_e32 v94, v46, v50
	v_sub_f32_e32 v93, v45, v50
	v_sub_f32_e32 v92, v44, v50
	v_sub_f32_e32 v91, v43, v50
	v_sub_f32_e32 v90, v42, v50
	v_sub_f32_e32 v89, v41, v50
	v_sub_f32_e32 v88, v40, v50
	v_sub_f32_e32 v87, v39, v50
	v_sub_f32_e32 v86, v38, v50
	v_sub_f32_e32 v85, v37, v50
	v_sub_f32_e32 v84, v36, v50
	v_sub_f32_e32 v83, v35, v50
	v_sub_f32_e32 v82, v34, v50
	v_lshl_add_u32 v204, v170, 6, 0
	v_cmp_gt_u32_e64 s[2:3], 32, v171
	v_lshl_add_u32 v192, v170, 2, s93
	v_lshl_add_u64 v[170:171], s[66:67], 0, v[18:19]
	v_mov_b64_e32 v[64:65], v[16:17]
	v_mov_b64_e32 v[48:49], v[16:17]
	v_mov_b64_e32 v[32:33], v[16:17]
	v_add_u32_e32 v191, s93, v98
	v_lshl_add_u64 v[172:173], v[166:167], 0, s[4:5]
	v_lshl_add_u64 v[174:175], s[4:5], 0, v[164:165]
	s_add_u32 s24, s0, 0x6000
	s_addc_u32 s25, s1, 0
	s_add_u32 s26, s6, 0x4e000040
	s_addc_u32 s27, s7, 0
	s_and_b32 s94, s64, 1
	s_cmp_eq_u32 s94, 0
	s_cbranch_scc0 .Lstg_pre_l0
	s_mov_b32 m0, s90
	s_nop 0
	global_load_lds_dwordx4 v164, s[24:25]
	s_mov_b32 m0, s88
	s_nop 0
	global_load_lds_dwordx4 v170, s[26:27]
	s_add_u32 s24, s24, 0x3000
	s_addc_u32 s25, s25, 0
	s_add_u32 s26, s26, 64
	s_addc_u32 s27, s27, 0
.Lstg_pre_l0:
	v_mov_b32_e32 v205, 1.0
	s_mov_b32 s9, -5
	v_mov_b64_e32 v[62:63], v[14:15]
	v_mov_b64_e32 v[60:61], v[12:13]
	v_mov_b64_e32 v[58:59], v[10:11]
	v_mov_b64_e32 v[56:57], v[8:9]
	v_mov_b64_e32 v[54:55], v[6:7]
	v_mov_b64_e32 v[52:53], v[4:5]
	v_mov_b64_e32 v[50:51], v[2:3]
	v_mov_b64_e32 v[46:47], v[14:15]
	v_mov_b64_e32 v[44:45], v[12:13]
	v_mov_b64_e32 v[42:43], v[10:11]
	v_mov_b64_e32 v[40:41], v[8:9]
	v_mov_b64_e32 v[38:39], v[6:7]
	v_mov_b64_e32 v[36:37], v[4:5]
	v_mov_b64_e32 v[34:35], v[2:3]
	v_mov_b64_e32 v[30:31], v[14:15]
	v_mov_b64_e32 v[28:29], v[12:13]
	v_mov_b64_e32 v[26:27], v[10:11]
	v_mov_b64_e32 v[24:25], v[8:9]
	v_mov_b64_e32 v[22:23], v[6:7]
	v_mov_b64_e32 v[20:21], v[4:5]
	v_mov_b64_e32 v[18:19], v[2:3]
	v_mov_b32_e32 v130, 0
	v_mov_b32_e32 v131, v162
	v_mov_b32_e32 v132, v162
	v_mov_b32_e32 v133, v162
	v_mov_b32_e32 v134, v162
	v_mov_b32_e32 v135, v162
	v_mov_b32_e32 v136, v162
	v_mov_b32_e32 v137, v162
.LBB0_887:
	v_cndmask_b32_e64 v98, 0, 1, s[64:65]
	v_cmp_ne_u32_e64 s[4:5], 1, v98
	s_cmp_eq_u32 s94, 0
	s_cbranch_scc1 .Lstg_top_l0
	s_mov_b32 m0, s90
	s_nop 0
	global_load_lds_dwordx4 v164, s[24:25]
	s_mov_b32 m0, s91
	s_nop 0
	global_load_lds_dwordx4 v166, s[24:25]
	s_mov_b32 m0, s88
	s_nop 0
	global_load_lds_dwordx4 v170, s[26:27]
	s_add_u32 s24, s24, 0x3000
	s_addc_u32 s25, s25, 0
	s_add_u32 s26, s26, 64
	s_addc_u32 s27, s27, 0
; __device__ __forceinline__ void finishSM(f32x16& p0, f32x16& p1, float alpha, float& l_reg, v8i& pa) {
; #pragma unroll
;   for (int r = 0; r < 16; ++r) p1[r] = __builtin_amdgcn_exp2f(p1[r]);
;   float ps = 0;
; #pragma unroll
;   for (int r = 0; r < 16; ++r) ps += p0[r];
; #pragma unroll
;   for (int r = 0; r < 16; ++r) ps += p1[r];
;   { auto rr = __builtin_amdgcn_permlane32_swap(__float_as_uint(ps), __float_as_uint(ps), false, false);
;     ps = __uint_as_float(rr[0]) + __uint_as_float(rr[1]); }
;   l_reg = l_reg * alpha + ps;
; #pragma unroll
;   for (int q = 0; q < 4; ++q) { int w0 = pa[q], w1 = pa[4 + q];
;     w0 = __builtin_amdgcn_cvt_pk_fp8_f32(p0[4 * q], p0[4 * q + 1], w0, false); w0 = __builtin_amdgcn_cvt_pk_fp8_f32(p0[4 * q + 2], p0[4 * q + 3], w0, true);
;     w1 = __builtin_amdgcn_cvt_pk_fp8_f32(p1[4 * q], p1[4 * q + 1], w1, false); w1 = __builtin_amdgcn_cvt_pk_fp8_f32(p1[4 * q + 2], p1[4 * q + 3], w1, true);
;     pa[q] = w0; pa[4 + q] = w1; }
; }
; __device__ __forceinline__ void qkt(f32x16& p0, f32x16& p1, const char* Ks, const v8i* qr, int r32, int hi, const f32x16& nm16) {
; #pragma unroll
;   for (int s = 0; s < 3; ++s) { const int c0 = 4 * s + 2 * hi;
;     const v8i a0 = __builtin_shufflevector(*reinterpret_cast<const v4i*>(Ks + k8_off(r32, c0)), *reinterpret_cast<const v4i*>(Ks + k8_off(r32, c0 + 1)), 0, 1, 2, 3, 4, 5, 6, 7);
;     const v8i a1 = __builtin_shufflevector(*reinterpret_cast<const v4i*>(Ks + 32 * DQK + k8_off(r32, c0)), *reinterpret_cast<const v4i*>(Ks + 32 * DQK + k8_off(r32, c0 + 1)), 0, 1, 2, 3, 4, 5, 6, 7);
;     p0 = __builtin_amdgcn_mfma_scale_f32_32x32x64_f8f6f4(a0, qr[s], s == 0 ? nm16 : p0, 0, 0, 0, 0, 0, 0);
;     p1 = __builtin_amdgcn_mfma_scale_f32_32x32x64_f8f6f4(a1, qr[s], s == 0 ? nm16 : p1, 0, 0, 0, 0, 0, 0); }
; }
; __device__ __forceinline__ void pv_d0(f32x16* o, const char* Vs, v8i pa, int r32, int hi) {
; #pragma unroll
;   for (int d0 = 0; d0 < 4; ++d0) { const int row = 32 * d0 + r32, x = (row >> 2) & 3;
;     const v8i vb = __builtin_shufflevector(*reinterpret_cast<const v4i*>(Vs + row * 64 + (((2 * hi) ^ x) << 4)), *reinterpret_cast<const v4i*>(Vs + row * 64 + (((2 * hi + 1) ^ x) << 4)), 0, 1, 2, 3, 4, 5, 6, 7);
;     o[d0] = __builtin_amdgcn_mfma_scale_f32_32x32x64_f8f6f4(pa, vb, o[d0], 0, 0, 0, 0, 0, 0); }
; }
.Lstg_top_l0:
	ds_read_b128 v[98:101], v196 offset:20480
	ds_read_b128 v[102:105], v197 offset:20480
	ds_read_b128 v[206:209], v196 offset:26624
	ds_read_b128 v[210:213], v197 offset:26624
	v_add_f32_e32 v182, 0, v235
	v_add_f32_e32 v182, v236, v182
	s_waitcnt lgkmcnt(0)
	v_mfma_f32_32x32x64_f8f6f4 v[114:129], v[98:105], v[138:145], v[66:81]
	v_add_f32_e32 v182, v233, v182
	v_add_f32_e32 v182, v234, v182
	v_add_f32_e32 v182, v231, v182
	v_add_f32_e32 v182, v232, v182
	v_add_f32_e32 v182, v229, v182
	v_add_f32_e32 v182, v230, v182
	v_add_f32_e32 v182, v227, v182
	v_add_f32_e32 v182, v228, v182
	v_add_f32_e32 v182, v225, v182
	v_add_f32_e32 v182, v226, v182
	v_exp_f32_e32 v82, v82
	v_add_f32_e32 v182, v223, v182
	v_exp_f32_e32 v83, v83
	v_add_f32_e32 v182, v224, v182
	v_exp_f32_e32 v84, v84
	v_mfma_f32_32x32x64_f8f6f4 v[98:113], v[206:213], v[138:145], v[66:81]
	ds_read_b128 v[206:209], v198 offset:20480
	ds_read_b128 v[210:213], v199 offset:20480
	ds_read_b128 v[238:241], v198 offset:26624
	ds_read_b128 v[242:245], v199 offset:26624
	v_add_f32_e32 v182, v221, v182
	v_exp_f32_e32 v85, v85
	v_add_f32_e32 v182, v222, v182
	v_exp_f32_e32 v86, v86
	v_add_f32_e32 v182, v82, v182
	v_exp_f32_e32 v87, v87
	v_add_f32_e32 v182, v83, v182
	v_exp_f32_e32 v88, v88
	v_add_f32_e32 v182, v84, v182
	v_exp_f32_e32 v89, v89
	v_add_f32_e32 v182, v85, v182
	v_exp_f32_e32 v90, v90
	v_add_f32_e32 v182, v86, v182
	v_exp_f32_e32 v91, v91
	s_waitcnt lgkmcnt(0)
	v_mfma_f32_32x32x64_f8f6f4 v[114:129], v[206:213], v[146:153], v[114:129]
	v_add_f32_e32 v182, v87, v182
	v_exp_f32_e32 v92, v92
	v_exp_f32_e32 v94, v94
	v_exp_f32_e32 v95, v95
	v_add_f32_e32 v182, v88, v182
	v_exp_f32_e32 v93, v93
	v_add_f32_e32 v182, v89, v182
	v_add_f32_e32 v182, v90, v182
	v_add_f32_e32 v182, v91, v182
	v_exp_f32_e32 v96, v96
	v_exp_f32_e32 v97, v97
	v_add_f32_e32 v182, v92, v182
	v_cvt_pk_fp8_f32 v130, v235, v236
	v_cvt_pk_fp8_f32 v134, v82, v83
	v_cvt_pk_fp8_f32 v131, v231, v232
	v_mfma_f32_32x32x64_f8f6f4 v[98:113], v[238:245], v[146:153], v[98:113]
	ds_read_b128 v[206:209], v200 offset:20480
	ds_read_b128 v[210:213], v201 offset:20480
	ds_read_b128 v[238:241], v200 offset:26624
	ds_read_b128 v[242:245], v201 offset:26624
	v_cvt_pk_fp8_f32 v135, v86, v87
	v_cvt_pk_fp8_f32 v132, v227, v228
	v_cvt_pk_fp8_f32 v136, v90, v91
	v_cvt_pk_fp8_f32 v133, v223, v224
	v_cvt_pk_fp8_f32 v137, v94, v95
	v_add_f32_e32 v182, v93, v182
	v_add_f32_e32 v182, v94, v182
	v_add_f32_e32 v182, v95, v182
	v_add_f32_e32 v182, v96, v182
	v_cvt_pk_fp8_f32 v130, v233, v234 op_sel:[0,0,1]
	v_cvt_pk_fp8_f32 v134, v84, v85 op_sel:[0,0,1]
	v_cvt_pk_fp8_f32 v131, v229, v230 op_sel:[0,0,1]
	v_cvt_pk_fp8_f32 v135, v88, v89 op_sel:[0,0,1]
	v_cvt_pk_fp8_f32 v132, v225, v226 op_sel:[0,0,1]
	s_waitcnt lgkmcnt(0)
	v_mfma_f32_32x32x64_f8f6f4 v[114:129], v[206:213], v[154:161], v[114:129]
	v_cvt_pk_fp8_f32 v136, v92, v93 op_sel:[0,0,1]
	v_cvt_pk_fp8_f32 v133, v221, v222 op_sel:[0,0,1]
	v_cvt_pk_fp8_f32 v137, v96, v97 op_sel:[0,0,1]
	v_add_f32_e32 v206, v97, v182
	v_mov_b32_e32 v207, v206
	s_nop 1
	v_permlane32_swap_b32_e32 v206, v207
	v_mfma_f32_32x32x64_f8f6f4 v[98:113], v[238:245], v[154:161], v[98:113]
	s_cmp_eq_u32 s94, 0
	s_cbranch_scc0 .Lstg_mid0_l0
	s_waitcnt vmcnt(0)
	s_barrier
	s_mov_b32 m0, s87
	s_nop 0
	global_load_lds_dwordx4 v164, s[24:25]
	s_mov_b32 m0, s89
	s_nop 0
	global_load_lds_dwordx4 v170, s[26:27]
	s_add_u32 s24, s24, 0x3000
	s_addc_u32 s25, s25, 0
	s_add_u32 s26, s26, 64
	s_addc_u32 s27, s27, 0
.Lstg_mid0_l0:
	v_add_u32_e32 v194, v204, v203
	v_add_u32_e32 v193, v204, v202
	ds_read_b128 v[86:89], v194
	ds_read_b128 v[82:85], v193
	ds_read_b128 v[90:93], v193 offset:2048
	ds_read_b128 v[94:97], v194 offset:2048
	s_nop 4
	v_max_f32_e32 v182, v115, v115
	v_max_f32_e32 v183, v114, v114
	v_max_f32_e32 v182, v183, v182
	s_waitcnt lgkmcnt(0)
	v_mfma_f32_32x32x64_f8f6f4 v[2:17], v[130:137], v[82:89], v[2:17]
	v_max3_f32 v182, v182, v116, v117
	v_max3_f32 v182, v182, v118, v119
	v_max3_f32 v182, v182, v120, v121
	v_max3_f32 v182, v182, v122, v123
	v_max3_f32 v182, v182, v124, v125
	v_max3_f32 v182, v182, v126, v127
	v_max3_f32 v182, v182, v128, v129
	v_max3_f32 v182, v182, v98, v99
	v_mov_b32_e32 v208, 1.0
	v_mfma_f32_32x32x64_f8f6f4 v[50:65], v[130:137], v[90:97], v[50:65]
	ds_read_b128 v[82:85], v193 offset:4096
	ds_read_b128 v[90:93], v193 offset:6144
	ds_read_b128 v[86:89], v194 offset:4096
	ds_read_b128 v[94:97], v194 offset:6144
	s_waitcnt lgkmcnt(0)
	v_mfma_f32_32x32x64_f8f6f4 v[34:49], v[130:137], v[82:89], v[34:49]
	v_max3_f32 v82, v182, v100, v101
	v_max3_f32 v82, v82, v102, v103
	v_max3_f32 v82, v82, v104, v105
	v_max3_f32 v82, v82, v106, v107
	v_max3_f32 v82, v82, v108, v109
	v_max3_f32 v82, v82, v110, v111
	v_max3_f32 v82, v82, v112, v113
	v_mov_b32_e32 v83, v82
	s_nop 1
	v_permlane32_swap_b32_e32 v82, v83
	v_max_f32_e32 v83, v83, v83
	v_max_f32_e32 v82, v82, v82
	v_max_f32_e32 v82, v82, v83
	v_cmp_ge_f32_e32 vcc, s85, v82
	s_cmp_eq_u64 vcc, exec
	v_mfma_f32_32x32x64_f8f6f4 v[18:33], v[130:137], v[90:97], v[18:33]
	s_cbranch_scc0 .LBB0_931
	v_cmp_gt_f32_e32 vcc, 1.0, v208
	s_cbranch_vccz .LBB0_894

; __device__ __forceinline__ void finishSM(f32x16& p0, f32x16& p1, float alpha, float& l_reg, v8i& pa) {
; #pragma unroll
;   for (int r = 0; r < 16; ++r) p1[r] = __builtin_amdgcn_exp2f(p1[r]);
;   float ps = 0;
; #pragma unroll
;   for (int r = 0; r < 16; ++r) ps += p0[r];
; #pragma unroll
;   for (int r = 0; r < 16; ++r) ps += p1[r];
;   { auto rr = __builtin_amdgcn_permlane32_swap(__float_as_uint(ps), __float_as_uint(ps), false, false);
;     ps = __uint_as_float(rr[0]) + __uint_as_float(rr[1]); }
;   l_reg = l_reg * alpha + ps;
; #pragma unroll
;   for (int q = 0; q < 4; ++q) { int w0 = pa[q], w1 = pa[4 + q];
;     w0 = __builtin_amdgcn_cvt_pk_fp8_f32(p0[4 * q], p0[4 * q + 1], w0, false); w0 = __builtin_amdgcn_cvt_pk_fp8_f32(p0[4 * q + 2], p0[4 * q + 3], w0, true);
;     w1 = __builtin_amdgcn_cvt_pk_fp8_f32(p1[4 * q], p1[4 * q + 1], w1, false); w1 = __builtin_amdgcn_cvt_pk_fp8_f32(p1[4 * q + 2], p1[4 * q + 3], w1, true);
;     pa[q] = w0; pa[4 + q] = w1; }
; }
; __device__ __forceinline__ void qkt(f32x16& p0, f32x16& p1, const char* Ks, const v8i* qr, int r32, int hi, const f32x16& nm16) {
; #pragma unroll
;   for (int s = 0; s < 3; ++s) { const int c0 = 4 * s + 2 * hi;
;     const v8i a0 = __builtin_shufflevector(*reinterpret_cast<const v4i*>(Ks + k8_off(r32, c0)), *reinterpret_cast<const v4i*>(Ks + k8_off(r32, c0 + 1)), 0, 1, 2, 3, 4, 5, 6, 7);
;     const v8i a1 = __builtin_shufflevector(*reinterpret_cast<const v4i*>(Ks + 32 * DQK + k8_off(r32, c0)), *reinterpret_cast<const v4i*>(Ks + 32 * DQK + k8_off(r32, c0 + 1)), 0, 1, 2, 3, 4, 5, 6, 7);
;     p0 = __builtin_amdgcn_mfma_scale_f32_32x32x64_f8f6f4(a0, qr[s], s == 0 ? nm16 : p0, 0, 0, 0, 0, 0, 0);
;     p1 = __builtin_amdgcn_mfma_scale_f32_32x32x64_f8f6f4(a1, qr[s], s == 0 ? nm16 : p1, 0, 0, 0, 0, 0, 0); }
; }
; __device__ __forceinline__ void pv_d0(f32x16* o, const char* Vs, v8i pa, int r32, int hi) {
; #pragma unroll
;   for (int d0 = 0; d0 < 4; ++d0) { const int row = 32 * d0 + r32, x = (row >> 2) & 3;
;     const v8i vb = __builtin_shufflevector(*reinterpret_cast<const v4i*>(Vs + row * 64 + (((2 * hi) ^ x) << 4)), *reinterpret_cast<const v4i*>(Vs + row * 64 + (((2 * hi + 1) ^ x) << 4)), 0, 1, 2, 3, 4, 5, 6, 7);
;     o[d0] = __builtin_amdgcn_mfma_scale_f32_32x32x64_f8f6f4(pa, vb, o[d0], 0, 0, 0, 0, 0, 0); }
; }
.LBB0_894:
	s_cmp_eq_u32 s94, 0
	s_cbranch_scc1 .Lstg_end0_l0
	s_waitcnt vmcnt(0)
	s_barrier
	s_mov_b32 m0, s87
	s_nop 0
	global_load_lds_dwordx4 v164, s[24:25]
	s_add_i32 m0, s86, 0x4000
	s_nop 0
	global_load_lds_dwordx4 v166, s[24:25]
	s_mov_b32 m0, s89
	s_nop 0
	global_load_lds_dwordx4 v170, s[26:27]
	s_add_u32 s24, s24, 0x3000
	s_addc_u32 s25, s25, 0
	s_add_u32 s26, s26, 64
	s_addc_u32 s27, s27, 0
.Lstg_end0_l0:
	v_exp_f32_e32 v182, v114
	v_exp_f32_e32 v183, v115
	v_exp_f32_e32 v184, v116
	v_exp_f32_e32 v185, v117
	v_exp_f32_e32 v226, v118
	v_exp_f32_e32 v227, v119
	v_exp_f32_e32 v228, v120
	v_exp_f32_e32 v229, v121
	v_exp_f32_e32 v230, v122
	v_exp_f32_e32 v231, v123
	v_exp_f32_e32 v232, v124
	v_exp_f32_e32 v233, v125
	v_exp_f32_e32 v234, v126
	v_exp_f32_e32 v235, v127
	v_exp_f32_e32 v236, v128
	v_exp_f32_e32 v237, v129
	ds_read_b128 v[82:85], v196 offset:49152
	ds_read_b128 v[86:89], v197 offset:49152
	ds_read_b128 v[210:213], v196 offset:55296
	ds_read_b128 v[214:217], v197 offset:55296
	v_add_f32_e32 v209, 0, v182
	v_add_f32_e32 v209, v183, v209
	s_waitcnt lgkmcnt(0)
	v_mfma_f32_32x32x64_f8f6f4 v[114:129], v[82:89], v[138:145], v[66:81]
	v_add_f32_e32 v209, v184, v209
	v_add_f32_e32 v209, v185, v209
	v_add_f32_e32 v209, v226, v209
	v_add_f32_e32 v209, v227, v209
	v_add_f32_e32 v209, v228, v209
	v_add_f32_e32 v209, v229, v209
	v_add_f32_e32 v209, v230, v209
	v_add_f32_e32 v209, v231, v209
	v_add_f32_e32 v209, v232, v209
	v_add_f32_e32 v209, v233, v209
	v_exp_f32_e32 v98, v98
	v_add_f32_e32 v209, v234, v209
	v_exp_f32_e32 v99, v99
	v_add_f32_e32 v209, v235, v209
	v_exp_f32_e32 v100, v100
	v_mfma_f32_32x32x64_f8f6f4 v[82:97], v[210:217], v[138:145], v[66:81]
	ds_read_b128 v[210:213], v198 offset:49152
	ds_read_b128 v[214:217], v199 offset:49152
	ds_read_b128 v[218:221], v198 offset:55296
	ds_read_b128 v[222:225], v199 offset:55296
	v_add_f32_e32 v209, v236, v209
	v_exp_f32_e32 v101, v101
	v_add_f32_e32 v209, v237, v209
	v_exp_f32_e32 v102, v102
	v_add_f32_e32 v209, v98, v209
	v_exp_f32_e32 v103, v103
	v_add_f32_e32 v209, v99, v209
	v_exp_f32_e32 v104, v104
	v_add_f32_e32 v209, v100, v209
	v_exp_f32_e32 v105, v105
	v_add_f32_e32 v209, v101, v209
	v_exp_f32_e32 v106, v106
	v_add_f32_e32 v209, v102, v209
	v_exp_f32_e32 v107, v107
	s_waitcnt lgkmcnt(0)
	v_mfma_f32_32x32x64_f8f6f4 v[114:129], v[210:217], v[146:153], v[114:129]
	v_add_f32_e32 v209, v103, v209
	v_exp_f32_e32 v108, v108
	v_exp_f32_e32 v110, v110
	v_exp_f32_e32 v111, v111
	v_add_f32_e32 v209, v104, v209
	v_exp_f32_e32 v109, v109
	v_add_f32_e32 v209, v105, v209
	v_add_f32_e32 v209, v106, v209
	v_add_f32_e32 v209, v107, v209
	v_exp_f32_e32 v112, v112
	v_exp_f32_e32 v113, v113
	v_add_f32_e32 v209, v108, v209
	v_cvt_pk_fp8_f32 v130, v182, v183
	v_cvt_pk_fp8_f32 v134, v98, v99
	v_cvt_pk_fp8_f32 v131, v226, v227
	v_mfma_f32_32x32x64_f8f6f4 v[82:97], v[218:225], v[146:153], v[82:97]
	ds_read_b128 v[210:213], v200 offset:49152
	ds_read_b128 v[214:217], v201 offset:49152
	ds_read_b128 v[218:221], v200 offset:55296
	ds_read_b128 v[222:225], v201 offset:55296
	v_cvt_pk_fp8_f32 v135, v102, v103
	v_cvt_pk_fp8_f32 v132, v230, v231
	v_cvt_pk_fp8_f32 v136, v106, v107
	v_cvt_pk_fp8_f32 v133, v234, v235
	v_cvt_pk_fp8_f32 v137, v110, v111
	v_add_f32_e32 v209, v109, v209
	v_add_f32_e32 v209, v110, v209
	v_add_f32_e32 v209, v111, v209
	v_add_f32_e32 v209, v112, v209
	v_cvt_pk_fp8_f32 v130, v184, v185 op_sel:[0,0,1]
	v_cvt_pk_fp8_f32 v134, v100, v101 op_sel:[0,0,1]
	v_cvt_pk_fp8_f32 v131, v228, v229 op_sel:[0,0,1]
	v_cvt_pk_fp8_f32 v135, v104, v105 op_sel:[0,0,1]
	v_cvt_pk_fp8_f32 v132, v232, v233 op_sel:[0,0,1]
	s_waitcnt lgkmcnt(0)
	v_mfma_f32_32x32x64_f8f6f4 v[114:129], v[210:217], v[154:161], v[114:129]
	v_cvt_pk_fp8_f32 v136, v108, v109 op_sel:[0,0,1]
	v_cvt_pk_fp8_f32 v133, v236, v237 op_sel:[0,0,1]
	v_cvt_pk_fp8_f32 v137, v112, v113 op_sel:[0,0,1]
	v_add_f32_e32 v209, v113, v209
	v_mov_b32_e32 v210, v209
	s_nop 1
	v_permlane32_swap_b32_e32 v209, v210
	v_mfma_f32_32x32x64_f8f6f4 v[82:97], v[218:225], v[154:161], v[82:97]
	s_cmp_eq_u32 s94, 0
	s_cbranch_scc0 .Lstg_mid1_l0
	s_waitcnt vmcnt(0)
	s_barrier
	s_mov_b32 m0, s92
	s_nop 0
	global_load_lds_dwordx4 v164, s[24:25]
	s_mov_b32 m0, s86
	s_nop 0
	global_load_lds_dwordx4 v170, s[26:27]
	s_add_u32 s24, s24, 0x3000
	s_addc_u32 s25, s25, 0
	s_add_u32 s26, s26, 64
	s_addc_u32 s27, s27, 0
.Lstg_mid1_l0:
	ds_read_b128 v[102:105], v194 offset:32768
	ds_read_b128 v[98:101], v193 offset:32768
	ds_read_b128 v[106:109], v193 offset:34816
	ds_read_b128 v[110:113], v194 offset:34816
	s_nop 6
	v_max_f32_e32 v182, v115, v115
	v_max_f32_e32 v183, v114, v114
	v_max_f32_e32 v182, v183, v182
	s_waitcnt lgkmcnt(0)
	v_mfma_f32_32x32x64_f8f6f4 v[2:17], v[130:137], v[98:105], v[2:17]
	v_max3_f32 v182, v182, v116, v117
	v_max3_f32 v182, v182, v118, v119
	v_max3_f32 v182, v182, v120, v121
	v_max3_f32 v182, v182, v122, v123
	v_max3_f32 v182, v182, v124, v125
	v_max3_f32 v182, v182, v126, v127
	v_max3_f32 v182, v182, v128, v129
	v_max3_f32 v182, v182, v82, v83
	v_mov_b32_e32 v211, 1.0
	v_mfma_f32_32x32x64_f8f6f4 v[50:65], v[130:137], v[106:113], v[50:65]
	ds_read_b128 v[98:101], v193 offset:36864
	ds_read_b128 v[106:109], v193 offset:38912
	ds_read_b128 v[102:105], v194 offset:36864
	ds_read_b128 v[110:113], v194 offset:38912
	s_waitcnt lgkmcnt(0)
	v_mfma_f32_32x32x64_f8f6f4 v[34:49], v[130:137], v[98:105], v[34:49]
	v_max3_f32 v98, v182, v84, v85
	v_max3_f32 v98, v98, v86, v87
	v_max3_f32 v98, v98, v88, v89
	v_max3_f32 v98, v98, v90, v91
	v_max3_f32 v98, v98, v92, v93
	v_max3_f32 v98, v98, v94, v95
	v_max3_f32 v98, v98, v96, v97
	v_mov_b32_e32 v99, v98
	s_nop 1
	v_permlane32_swap_b32_e32 v98, v99
	v_max_f32_e32 v99, v99, v99
	v_max_f32_e32 v98, v98, v98
	v_max_f32_e32 v98, v98, v99
	v_cmp_ge_f32_e32 vcc, s85, v98
	s_cmp_eq_u64 vcc, exec
	v_mfma_f32_32x32x64_f8f6f4 v[18:33], v[130:137], v[106:113], v[18:33]
	s_cbranch_scc0 .LBB0_932
	v_cmp_gt_f32_e32 vcc, 1.0, v211
	s_cbranch_vccz .LBB0_901

; __device__ __forceinline__ void finishSM(f32x16& p0, f32x16& p1, float alpha, float& l_reg, v8i& pa) {
; #pragma unroll
;   for (int r = 0; r < 16; ++r) p1[r] = __builtin_amdgcn_exp2f(p1[r]);
;   float ps = 0;
; #pragma unroll
;   for (int r = 0; r < 16; ++r) ps += p0[r];
; #pragma unroll
;   for (int r = 0; r < 16; ++r) ps += p1[r];
;   { auto rr = __builtin_amdgcn_permlane32_swap(__float_as_uint(ps), __float_as_uint(ps), false, false);
;     ps = __uint_as_float(rr[0]) + __uint_as_float(rr[1]); }
;   l_reg = l_reg * alpha + ps;
; #pragma unroll
;   for (int q = 0; q < 4; ++q) { int w0 = pa[q], w1 = pa[4 + q];
;     w0 = __builtin_amdgcn_cvt_pk_fp8_f32(p0[4 * q], p0[4 * q + 1], w0, false); w0 = __builtin_amdgcn_cvt_pk_fp8_f32(p0[4 * q + 2], p0[4 * q + 3], w0, true);
;     w1 = __builtin_amdgcn_cvt_pk_fp8_f32(p1[4 * q], p1[4 * q + 1], w1, false); w1 = __builtin_amdgcn_cvt_pk_fp8_f32(p1[4 * q + 2], p1[4 * q + 3], w1, true);
;     pa[q] = w0; pa[4 + q] = w1; }
; }
; __device__ __forceinline__ void qkt(f32x16& p0, f32x16& p1, const char* Ks, const v8i* qr, int r32, int hi, const f32x16& nm16) {
; #pragma unroll
;   for (int s = 0; s < 3; ++s) { const int c0 = 4 * s + 2 * hi;
;     const v8i a0 = __builtin_shufflevector(*reinterpret_cast<const v4i*>(Ks + k8_off(r32, c0)), *reinterpret_cast<const v4i*>(Ks + k8_off(r32, c0 + 1)), 0, 1, 2, 3, 4, 5, 6, 7);
;     const v8i a1 = __builtin_shufflevector(*reinterpret_cast<const v4i*>(Ks + 32 * DQK + k8_off(r32, c0)), *reinterpret_cast<const v4i*>(Ks + 32 * DQK + k8_off(r32, c0 + 1)), 0, 1, 2, 3, 4, 5, 6, 7);
;     p0 = __builtin_amdgcn_mfma_scale_f32_32x32x64_f8f6f4(a0, qr[s], s == 0 ? nm16 : p0, 0, 0, 0, 0, 0, 0);
;     p1 = __builtin_amdgcn_mfma_scale_f32_32x32x64_f8f6f4(a1, qr[s], s == 0 ? nm16 : p1, 0, 0, 0, 0, 0, 0); }
; }
; __device__ __forceinline__ void pv_d0(f32x16* o, const char* Vs, v8i pa, int r32, int hi) {
; #pragma unroll
;   for (int d0 = 0; d0 < 4; ++d0) { const int row = 32 * d0 + r32, x = (row >> 2) & 3;
;     const v8i vb = __builtin_shufflevector(*reinterpret_cast<const v4i*>(Vs + row * 64 + (((2 * hi) ^ x) << 4)), *reinterpret_cast<const v4i*>(Vs + row * 64 + (((2 * hi + 1) ^ x) << 4)), 0, 1, 2, 3, 4, 5, 6, 7);
;     o[d0] = __builtin_amdgcn_mfma_scale_f32_32x32x64_f8f6f4(pa, vb, o[d0], 0, 0, 0, 0, 0, 0); }
; }
.LBB0_901:
	s_cmp_eq_u32 s94, 0
	s_cbranch_scc1 .Lstg_end1_l0
	s_waitcnt vmcnt(0)
	s_barrier
	s_mov_b32 m0, s92
	s_nop 0
	global_load_lds_dwordx4 v164, s[24:25]
	s_add_i32 m0, s86, 0x7000
	s_nop 0
	global_load_lds_dwordx4 v166, s[24:25]
	s_mov_b32 m0, s86
	s_nop 0
	global_load_lds_dwordx4 v170, s[26:27]
	s_add_u32 s24, s24, 0x3000
	s_addc_u32 s25, s25, 0
	s_add_u32 s26, s26, 64
	s_addc_u32 s27, s27, 0
.Lstg_end1_l0:
	v_exp_f32_e32 v182, v114
	v_exp_f32_e32 v183, v115
	v_exp_f32_e32 v184, v116
	v_exp_f32_e32 v185, v117
	v_exp_f32_e32 v228, v118
	v_exp_f32_e32 v229, v119
	v_exp_f32_e32 v230, v120
	v_exp_f32_e32 v231, v121
	v_exp_f32_e32 v232, v122
	v_exp_f32_e32 v233, v123
	v_exp_f32_e32 v234, v124
	v_exp_f32_e32 v235, v125
	v_exp_f32_e32 v236, v126
	v_exp_f32_e32 v237, v127
	v_exp_f32_e32 v238, v128
	v_exp_f32_e32 v239, v129
	ds_read_b128 v[98:101], v196 offset:8192
	ds_read_b128 v[102:105], v197 offset:8192
	ds_read_b128 v[212:215], v196 offset:14336
	ds_read_b128 v[216:219], v197 offset:14336
	v_exp_f32_e32 v82, v82
	v_exp_f32_e32 v83, v83
	s_waitcnt lgkmcnt(0)
	v_mfma_f32_32x32x64_f8f6f4 v[114:129], v[98:105], v[138:145], v[66:81]
	v_exp_f32_e32 v84, v84
	v_exp_f32_e32 v85, v85
	v_exp_f32_e32 v86, v86
	v_exp_f32_e32 v87, v87
	v_exp_f32_e32 v88, v88
	v_exp_f32_e32 v89, v89
	v_exp_f32_e32 v90, v90
	v_exp_f32_e32 v91, v91
	v_exp_f32_e32 v92, v92
	v_exp_f32_e32 v94, v94
	v_exp_f32_e32 v95, v95
	v_exp_f32_e32 v93, v93
	v_exp_f32_e32 v96, v96
	v_exp_f32_e32 v97, v97
	v_cvt_pk_fp8_f32 v130, v182, v183
	v_mfma_f32_32x32x64_f8f6f4 v[98:113], v[212:219], v[138:145], v[66:81]
	ds_read_b128 v[212:215], v198 offset:8192
	ds_read_b128 v[216:219], v199 offset:8192
	ds_read_b128 v[220:223], v198 offset:14336
	ds_read_b128 v[224:227], v199 offset:14336
	v_cvt_pk_fp8_f32 v134, v82, v83
	v_cvt_pk_fp8_f32 v131, v228, v229
	v_cvt_pk_fp8_f32 v135, v86, v87
	v_cvt_pk_fp8_f32 v132, v232, v233
	v_cvt_pk_fp8_f32 v136, v90, v91
	v_cvt_pk_fp8_f32 v133, v236, v237
	v_cvt_pk_fp8_f32 v137, v94, v95
	v_cvt_pk_fp8_f32 v130, v184, v185 op_sel:[0,0,1]
	v_cvt_pk_fp8_f32 v134, v84, v85 op_sel:[0,0,1]
	v_cvt_pk_fp8_f32 v131, v230, v231 op_sel:[0,0,1]
	v_cvt_pk_fp8_f32 v135, v88, v89 op_sel:[0,0,1]
	v_cvt_pk_fp8_f32 v132, v234, v235 op_sel:[0,0,1]
	v_cvt_pk_fp8_f32 v136, v92, v93 op_sel:[0,0,1]
	v_cvt_pk_fp8_f32 v133, v238, v239 op_sel:[0,0,1]
	s_waitcnt lgkmcnt(0)
	v_mfma_f32_32x32x64_f8f6f4 v[114:129], v[212:219], v[146:153], v[114:129]
	v_cvt_pk_fp8_f32 v137, v96, v97 op_sel:[0,0,1]
	v_mfma_f32_32x32x64_f8f6f4 v[98:113], v[220:227], v[146:153], v[98:113]
	ds_read_b128 v[212:215], v200 offset:8192
	ds_read_b128 v[216:219], v201 offset:8192
	ds_read_b128 v[220:223], v200 offset:14336
	ds_read_b128 v[224:227], v201 offset:14336
	s_waitcnt lgkmcnt(0)
	v_mfma_f32_32x32x64_f8f6f4 v[114:129], v[212:219], v[154:161], v[114:129]
	v_add_f32_e32 v212, 0, v182
	v_add_f32_e32 v212, v183, v212
	v_add_f32_e32 v212, v184, v212
	v_add_f32_e32 v212, v185, v212
	v_add_f32_e32 v212, v228, v212
	v_add_f32_e32 v212, v229, v212
	v_add_f32_e32 v212, v230, v212
	v_add_f32_e32 v212, v231, v212
	v_add_f32_e32 v212, v232, v212
	v_add_f32_e32 v212, v233, v212
	v_add_f32_e32 v212, v234, v212
	v_add_f32_e32 v212, v235, v212
	v_add_f32_e32 v212, v236, v212
	v_add_f32_e32 v212, v237, v212
	v_add_f32_e32 v212, v238, v212
	v_add_f32_e32 v212, v239, v212
	v_add_f32_e32 v212, v82, v212
	v_add_f32_e32 v212, v83, v212
	v_mfma_f32_32x32x64_f8f6f4 v[98:113], v[220:227], v[154:161], v[98:113]
	v_add_f32_e32 v212, v84, v212
	v_add_f32_e32 v212, v85, v212
	v_add_f32_e32 v212, v86, v212
	v_add_f32_e32 v212, v87, v212
	v_add_f32_e32 v212, v88, v212
	v_add_f32_e32 v212, v89, v212
	v_add_f32_e32 v212, v90, v212
	v_add_f32_e32 v212, v91, v212
	v_add_f32_e32 v212, v92, v212
	v_add_f32_e32 v212, v93, v212
	v_add_f32_e32 v212, v94, v212
	v_add_f32_e32 v212, v95, v212
	v_add_f32_e32 v212, v96, v212
	v_add_f32_e32 v212, v97, v212
	v_mov_b32_e32 v213, v212
	s_nop 1
	v_permlane32_swap_b32_e32 v212, v213
	s_cmp_eq_u32 s94, 0
	s_cbranch_scc0 .Lstg_mid2_l0
	s_waitcnt vmcnt(0)
	s_barrier
	s_mov_b32 m0, s90
	s_nop 0
	global_load_lds_dwordx4 v164, s[24:25]
	s_mov_b32 m0, s88
	s_nop 0
	global_load_lds_dwordx4 v170, s[26:27]
	s_add_u32 s24, s24, 0x3000
	s_addc_u32 s25, s25, 0
	s_add_u32 s26, s26, 64
	s_addc_u32 s27, s27, 0
.Lstg_mid2_l0:
	ds_read_b128 v[86:89], v194 offset:40960
	ds_read_b128 v[82:85], v193 offset:40960
	ds_read_b128 v[90:93], v193 offset:43008
	ds_read_b128 v[94:97], v194 offset:43008
	v_max_f32_e32 v182, v115, v115
	v_max_f32_e32 v183, v114, v114
	v_max_f32_e32 v182, v183, v182
	s_waitcnt lgkmcnt(0)
	v_mfma_f32_32x32x64_f8f6f4 v[2:17], v[130:137], v[82:89], v[2:17]
	v_max3_f32 v182, v182, v116, v117
	v_max3_f32 v182, v182, v118, v119
	v_max3_f32 v182, v182, v120, v121
	v_max3_f32 v182, v182, v122, v123
	v_max3_f32 v182, v182, v124, v125
	v_max3_f32 v182, v182, v126, v127
	v_max3_f32 v182, v182, v128, v129
	v_max3_f32 v182, v182, v98, v99
	v_mov_b32_e32 v214, 1.0
	v_mfma_f32_32x32x64_f8f6f4 v[50:65], v[130:137], v[90:97], v[50:65]
	ds_read_b128 v[82:85], v193 offset:45056
	ds_read_b128 v[90:93], v193 offset:47104
	ds_read_b128 v[86:89], v194 offset:45056
	ds_read_b128 v[94:97], v194 offset:47104
	s_waitcnt lgkmcnt(0)
	v_mfma_f32_32x32x64_f8f6f4 v[34:49], v[130:137], v[82:89], v[34:49]
	v_max3_f32 v82, v182, v100, v101
	v_max3_f32 v82, v82, v102, v103
	v_max3_f32 v82, v82, v104, v105
	v_max3_f32 v82, v82, v106, v107
	v_max3_f32 v82, v82, v108, v109
	v_max3_f32 v82, v82, v110, v111
	v_max3_f32 v82, v82, v112, v113
	v_mov_b32_e32 v83, v82
	s_nop 1
	v_permlane32_swap_b32_e32 v82, v83
	v_max_f32_e32 v83, v83, v83
	v_max_f32_e32 v82, v82, v82
	v_max_f32_e32 v82, v82, v83
	v_cmp_ge_f32_e32 vcc, s85, v82
	s_cmp_eq_u64 vcc, exec
	v_mfma_f32_32x32x64_f8f6f4 v[18:33], v[130:137], v[90:97], v[18:33]
	s_cbranch_scc0 .LBB0_933
	v_cmp_gt_f32_e32 vcc, 1.0, v214
	s_cbranch_vccz .LBB0_908

; __device__ __forceinline__ void finishSM(f32x16& p0, f32x16& p1, float alpha, float& l_reg, v8i& pa) {
; #pragma unroll
;   for (int r = 0; r < 16; ++r) p1[r] = __builtin_amdgcn_exp2f(p1[r]);
;   float ps = 0;
; #pragma unroll
;   for (int r = 0; r < 16; ++r) ps += p0[r];
; #pragma unroll
;   for (int r = 0; r < 16; ++r) ps += p1[r];
;   { auto rr = __builtin_amdgcn_permlane32_swap(__float_as_uint(ps), __float_as_uint(ps), false, false);
;     ps = __uint_as_float(rr[0]) + __uint_as_float(rr[1]); }
;   l_reg = l_reg * alpha + ps;
; #pragma unroll
;   for (int q = 0; q < 4; ++q) { int w0 = pa[q], w1 = pa[4 + q];
;     w0 = __builtin_amdgcn_cvt_pk_fp8_f32(p0[4 * q], p0[4 * q + 1], w0, false); w0 = __builtin_amdgcn_cvt_pk_fp8_f32(p0[4 * q + 2], p0[4 * q + 3], w0, true);
;     w1 = __builtin_amdgcn_cvt_pk_fp8_f32(p1[4 * q], p1[4 * q + 1], w1, false); w1 = __builtin_amdgcn_cvt_pk_fp8_f32(p1[4 * q + 2], p1[4 * q + 3], w1, true);
;     pa[q] = w0; pa[4 + q] = w1; }
; }
; __device__ __forceinline__ void qkt(f32x16& p0, f32x16& p1, const char* Ks, const v8i* qr, int r32, int hi, const f32x16& nm16) {
; #pragma unroll
;   for (int s = 0; s < 3; ++s) { const int c0 = 4 * s + 2 * hi;
;     const v8i a0 = __builtin_shufflevector(*reinterpret_cast<const v4i*>(Ks + k8_off(r32, c0)), *reinterpret_cast<const v4i*>(Ks + k8_off(r32, c0 + 1)), 0, 1, 2, 3, 4, 5, 6, 7);
;     const v8i a1 = __builtin_shufflevector(*reinterpret_cast<const v4i*>(Ks + 32 * DQK + k8_off(r32, c0)), *reinterpret_cast<const v4i*>(Ks + 32 * DQK + k8_off(r32, c0 + 1)), 0, 1, 2, 3, 4, 5, 6, 7);
;     p0 = __builtin_amdgcn_mfma_scale_f32_32x32x64_f8f6f4(a0, qr[s], s == 0 ? nm16 : p0, 0, 0, 0, 0, 0, 0);
;     p1 = __builtin_amdgcn_mfma_scale_f32_32x32x64_f8f6f4(a1, qr[s], s == 0 ? nm16 : p1, 0, 0, 0, 0, 0, 0); }
; }
; __device__ __forceinline__ void pv_d0(f32x16* o, const char* Vs, v8i pa, int r32, int hi) {
; #pragma unroll
;   for (int d0 = 0; d0 < 4; ++d0) { const int row = 32 * d0 + r32, x = (row >> 2) & 3;
;     const v8i vb = __builtin_shufflevector(*reinterpret_cast<const v4i*>(Vs + row * 64 + (((2 * hi) ^ x) << 4)), *reinterpret_cast<const v4i*>(Vs + row * 64 + (((2 * hi + 1) ^ x) << 4)), 0, 1, 2, 3, 4, 5, 6, 7);
;     o[d0] = __builtin_amdgcn_mfma_scale_f32_32x32x64_f8f6f4(pa, vb, o[d0], 0, 0, 0, 0, 0, 0); }
; }
.LBB0_908:
	s_cmp_eq_u32 s94, 0
	s_cbranch_scc1 .Lstg_end2_l0
	s_waitcnt vmcnt(0)
	s_barrier
	s_mov_b32 m0, s90
	s_nop 0
	global_load_lds_dwordx4 v164, s[24:25]
	s_mov_b32 m0, s91
	s_nop 0
	global_load_lds_dwordx4 v166, s[24:25]
	s_mov_b32 m0, s88
	s_nop 0
	global_load_lds_dwordx4 v170, s[26:27]
	s_add_u32 s24, s24, 0x3000
	s_addc_u32 s25, s25, 0
	s_add_u32 s26, s26, 64
	s_addc_u32 s27, s27, 0
.Lstg_end2_l0:
	v_exp_f32_e32 v182, v114
	v_exp_f32_e32 v183, v115
	v_exp_f32_e32 v184, v116
	v_exp_f32_e32 v185, v117
	v_exp_f32_e32 v232, v118
	v_exp_f32_e32 v233, v119
	v_exp_f32_e32 v234, v120
	v_exp_f32_e32 v235, v121
	v_exp_f32_e32 v236, v122
	v_exp_f32_e32 v237, v123
	v_exp_f32_e32 v238, v124
	v_exp_f32_e32 v239, v125
	v_exp_f32_e32 v240, v126
	v_exp_f32_e32 v241, v127
	v_exp_f32_e32 v242, v128
	v_exp_f32_e32 v243, v129
	ds_read_b128 v[82:85], v196 offset:20480
	ds_read_b128 v[86:89], v197 offset:20480
	ds_read_b128 v[216:219], v196 offset:26624
	ds_read_b128 v[220:223], v197 offset:26624
	v_add_f32_e32 v215, 0, v182
	v_add_f32_e32 v215, v183, v215
	s_waitcnt lgkmcnt(0)
	v_mfma_f32_32x32x64_f8f6f4 v[114:129], v[82:89], v[138:145], v[66:81]
	v_add_f32_e32 v215, v184, v215
	v_add_f32_e32 v215, v185, v215
	v_add_f32_e32 v215, v232, v215
	v_add_f32_e32 v215, v233, v215
	v_add_f32_e32 v215, v234, v215
	v_add_f32_e32 v215, v235, v215
	v_add_f32_e32 v215, v236, v215
	v_add_f32_e32 v215, v237, v215
	v_add_f32_e32 v215, v238, v215
	v_add_f32_e32 v215, v239, v215
	v_exp_f32_e32 v98, v98
	v_add_f32_e32 v215, v240, v215
	v_exp_f32_e32 v99, v99
	v_add_f32_e32 v215, v241, v215
	v_exp_f32_e32 v100, v100
	v_mfma_f32_32x32x64_f8f6f4 v[82:97], v[216:223], v[138:145], v[66:81]
	ds_read_b128 v[216:219], v198 offset:20480
	ds_read_b128 v[220:223], v199 offset:20480
	ds_read_b128 v[224:227], v198 offset:26624
	ds_read_b128 v[228:231], v199 offset:26624
	v_add_f32_e32 v215, v242, v215
	v_exp_f32_e32 v101, v101
	v_add_f32_e32 v215, v243, v215
	v_exp_f32_e32 v102, v102
	v_add_f32_e32 v215, v98, v215
	v_exp_f32_e32 v103, v103
	v_add_f32_e32 v215, v99, v215
	v_exp_f32_e32 v104, v104
	v_add_f32_e32 v215, v100, v215
	v_exp_f32_e32 v105, v105
	v_add_f32_e32 v215, v101, v215
	v_exp_f32_e32 v106, v106
	v_add_f32_e32 v215, v102, v215
	v_exp_f32_e32 v107, v107
	s_waitcnt lgkmcnt(0)
	v_mfma_f32_32x32x64_f8f6f4 v[114:129], v[216:223], v[146:153], v[114:129]
	v_add_f32_e32 v215, v103, v215
	v_exp_f32_e32 v108, v108
	v_exp_f32_e32 v110, v110
	v_exp_f32_e32 v111, v111
	v_add_f32_e32 v215, v104, v215
	v_exp_f32_e32 v109, v109
	v_add_f32_e32 v215, v105, v215
	v_add_f32_e32 v215, v106, v215
	v_add_f32_e32 v215, v107, v215
	v_exp_f32_e32 v112, v112
	v_exp_f32_e32 v113, v113
	v_add_f32_e32 v215, v108, v215
	v_cvt_pk_fp8_f32 v130, v182, v183
	v_cvt_pk_fp8_f32 v134, v98, v99
	v_cvt_pk_fp8_f32 v131, v232, v233
	v_mfma_f32_32x32x64_f8f6f4 v[82:97], v[224:231], v[146:153], v[82:97]
	ds_read_b128 v[216:219], v200 offset:20480
	ds_read_b128 v[220:223], v201 offset:20480
	ds_read_b128 v[224:227], v200 offset:26624
	ds_read_b128 v[228:231], v201 offset:26624
	v_cvt_pk_fp8_f32 v135, v102, v103
	v_cvt_pk_fp8_f32 v132, v236, v237
	v_cvt_pk_fp8_f32 v136, v106, v107
	v_cvt_pk_fp8_f32 v133, v240, v241
	v_cvt_pk_fp8_f32 v137, v110, v111
	v_add_f32_e32 v215, v109, v215
	v_add_f32_e32 v215, v110, v215
	v_add_f32_e32 v215, v111, v215
	v_add_f32_e32 v215, v112, v215
	v_cvt_pk_fp8_f32 v130, v184, v185 op_sel:[0,0,1]
	v_cvt_pk_fp8_f32 v134, v100, v101 op_sel:[0,0,1]
	v_cvt_pk_fp8_f32 v131, v234, v235 op_sel:[0,0,1]
	v_cvt_pk_fp8_f32 v135, v104, v105 op_sel:[0,0,1]
	v_cvt_pk_fp8_f32 v132, v238, v239 op_sel:[0,0,1]
	s_waitcnt lgkmcnt(0)
	v_mfma_f32_32x32x64_f8f6f4 v[114:129], v[216:223], v[154:161], v[114:129]
	v_cvt_pk_fp8_f32 v136, v108, v109 op_sel:[0,0,1]
	v_cvt_pk_fp8_f32 v133, v242, v243 op_sel:[0,0,1]
	v_cvt_pk_fp8_f32 v137, v112, v113 op_sel:[0,0,1]
	v_add_f32_e32 v215, v113, v215
	v_mov_b32_e32 v216, v215
	s_nop 1
	v_permlane32_swap_b32_e32 v215, v216
	v_mfma_f32_32x32x64_f8f6f4 v[82:97], v[224:231], v[154:161], v[82:97]
	s_cmp_eq_u32 s94, 0
	s_cbranch_scc0 .Lstg_mid3_l0
	s_waitcnt vmcnt(0)
	s_barrier
	s_mov_b32 m0, s87
	s_nop 0
	global_load_lds_dwordx4 v164, s[24:25]
	s_mov_b32 m0, s89
	s_nop 0
	global_load_lds_dwordx4 v170, s[26:27]
	s_add_u32 s24, s24, 0x3000
	s_addc_u32 s25, s25, 0
	s_add_u32 s26, s26, 64
	s_addc_u32 s27, s27, 0
.Lstg_mid3_l0:
	ds_read_b128 v[102:105], v194
	ds_read_b128 v[98:101], v193
	ds_read_b128 v[106:109], v193 offset:2048
	ds_read_b128 v[110:113], v194 offset:2048
	s_nop 6
	v_max_f32_e32 v182, v115, v115
	v_max_f32_e32 v183, v114, v114
	v_max_f32_e32 v182, v183, v182
	s_waitcnt lgkmcnt(0)
	v_mfma_f32_32x32x64_f8f6f4 v[2:17], v[130:137], v[98:105], v[2:17]
	v_max3_f32 v182, v182, v116, v117
	v_max3_f32 v182, v182, v118, v119
	v_max3_f32 v182, v182, v120, v121
	v_max3_f32 v182, v182, v122, v123
	v_max3_f32 v182, v182, v124, v125
	v_max3_f32 v182, v182, v126, v127
	v_max3_f32 v182, v182, v128, v129
	v_max3_f32 v182, v182, v82, v83
	v_mov_b32_e32 v217, 1.0
	v_mfma_f32_32x32x64_f8f6f4 v[50:65], v[130:137], v[106:113], v[50:65]
	ds_read_b128 v[98:101], v193 offset:4096
	ds_read_b128 v[106:109], v193 offset:6144
	ds_read_b128 v[102:105], v194 offset:4096
	ds_read_b128 v[110:113], v194 offset:6144
	s_waitcnt lgkmcnt(0)
	v_mfma_f32_32x32x64_f8f6f4 v[34:49], v[130:137], v[98:105], v[34:49]
	v_max3_f32 v98, v182, v84, v85
	v_max3_f32 v98, v98, v86, v87
	v_max3_f32 v98, v98, v88, v89
	v_max3_f32 v98, v98, v90, v91
	v_max3_f32 v98, v98, v92, v93
	v_max3_f32 v98, v98, v94, v95
	v_max3_f32 v98, v98, v96, v97
	v_mov_b32_e32 v99, v98
	s_nop 1
	v_permlane32_swap_b32_e32 v98, v99
	v_max_f32_e32 v99, v99, v99
	v_max_f32_e32 v98, v98, v98
	v_max_f32_e32 v98, v98, v99
	v_cmp_ge_f32_e32 vcc, s85, v98
	s_cmp_eq_u64 vcc, exec
	v_mfma_f32_32x32x64_f8f6f4 v[18:33], v[130:137], v[106:113], v[18:33]
	s_cbranch_scc0 .LBB0_934
	v_cmp_gt_f32_e32 vcc, 1.0, v217
	s_cbranch_vccz .LBB0_915

; __device__ __forceinline__ void finishSM(f32x16& p0, f32x16& p1, float alpha, float& l_reg, v8i& pa) {
; #pragma unroll
;   for (int r = 0; r < 16; ++r) p1[r] = __builtin_amdgcn_exp2f(p1[r]);
;   float ps = 0;
; #pragma unroll
;   for (int r = 0; r < 16; ++r) ps += p0[r];
; #pragma unroll
;   for (int r = 0; r < 16; ++r) ps += p1[r];
;   { auto rr = __builtin_amdgcn_permlane32_swap(__float_as_uint(ps), __float_as_uint(ps), false, false);
;     ps = __uint_as_float(rr[0]) + __uint_as_float(rr[1]); }
;   l_reg = l_reg * alpha + ps;
; #pragma unroll
;   for (int q = 0; q < 4; ++q) { int w0 = pa[q], w1 = pa[4 + q];
;     w0 = __builtin_amdgcn_cvt_pk_fp8_f32(p0[4 * q], p0[4 * q + 1], w0, false); w0 = __builtin_amdgcn_cvt_pk_fp8_f32(p0[4 * q + 2], p0[4 * q + 3], w0, true);
;     w1 = __builtin_amdgcn_cvt_pk_fp8_f32(p1[4 * q], p1[4 * q + 1], w1, false); w1 = __builtin_amdgcn_cvt_pk_fp8_f32(p1[4 * q + 2], p1[4 * q + 3], w1, true);
;     pa[q] = w0; pa[4 + q] = w1; }
; }
; __device__ __forceinline__ void qkt(f32x16& p0, f32x16& p1, const char* Ks, const v8i* qr, int r32, int hi, const f32x16& nm16) {
; #pragma unroll
;   for (int s = 0; s < 3; ++s) { const int c0 = 4 * s + 2 * hi;
;     const v8i a0 = __builtin_shufflevector(*reinterpret_cast<const v4i*>(Ks + k8_off(r32, c0)), *reinterpret_cast<const v4i*>(Ks + k8_off(r32, c0 + 1)), 0, 1, 2, 3, 4, 5, 6, 7);
;     const v8i a1 = __builtin_shufflevector(*reinterpret_cast<const v4i*>(Ks + 32 * DQK + k8_off(r32, c0)), *reinterpret_cast<const v4i*>(Ks + 32 * DQK + k8_off(r32, c0 + 1)), 0, 1, 2, 3, 4, 5, 6, 7);
;     p0 = __builtin_amdgcn_mfma_scale_f32_32x32x64_f8f6f4(a0, qr[s], s == 0 ? nm16 : p0, 0, 0, 0, 0, 0, 0);
;     p1 = __builtin_amdgcn_mfma_scale_f32_32x32x64_f8f6f4(a1, qr[s], s == 0 ? nm16 : p1, 0, 0, 0, 0, 0, 0); }
; }
; __device__ __forceinline__ void pv_d0(f32x16* o, const char* Vs, v8i pa, int r32, int hi) {
; #pragma unroll
;   for (int d0 = 0; d0 < 4; ++d0) { const int row = 32 * d0 + r32, x = (row >> 2) & 3;
;     const v8i vb = __builtin_shufflevector(*reinterpret_cast<const v4i*>(Vs + row * 64 + (((2 * hi) ^ x) << 4)), *reinterpret_cast<const v4i*>(Vs + row * 64 + (((2 * hi + 1) ^ x) << 4)), 0, 1, 2, 3, 4, 5, 6, 7);
;     o[d0] = __builtin_amdgcn_mfma_scale_f32_32x32x64_f8f6f4(pa, vb, o[d0], 0, 0, 0, 0, 0, 0); }
; }
.Lstg_end3_l0:
	v_exp_f32_e32 v182, v114
	v_exp_f32_e32 v183, v115
	v_exp_f32_e32 v184, v116
	v_exp_f32_e32 v185, v117
	v_exp_f32_e32 v234, v118
	v_exp_f32_e32 v235, v119
	v_exp_f32_e32 v236, v120
	v_exp_f32_e32 v237, v121
	v_exp_f32_e32 v238, v122
	v_exp_f32_e32 v239, v123
	v_exp_f32_e32 v240, v124
	v_exp_f32_e32 v241, v125
	v_exp_f32_e32 v242, v126
	v_exp_f32_e32 v243, v127
	v_exp_f32_e32 v244, v128
	v_exp_f32_e32 v245, v129
	ds_read_b128 v[98:101], v196 offset:49152
	ds_read_b128 v[102:105], v197 offset:49152
	ds_read_b128 v[218:221], v196 offset:55296
	ds_read_b128 v[222:225], v197 offset:55296
	v_exp_f32_e32 v82, v82
	v_exp_f32_e32 v83, v83
	s_waitcnt lgkmcnt(0)
	v_mfma_f32_32x32x64_f8f6f4 v[114:129], v[98:105], v[138:145], v[66:81]
	v_exp_f32_e32 v84, v84
	v_exp_f32_e32 v85, v85
	v_exp_f32_e32 v86, v86
	v_exp_f32_e32 v87, v87
	v_exp_f32_e32 v88, v88
	v_exp_f32_e32 v89, v89
	v_exp_f32_e32 v90, v90
	v_exp_f32_e32 v91, v91
	v_exp_f32_e32 v92, v92
	v_exp_f32_e32 v94, v94
	v_exp_f32_e32 v95, v95
	v_exp_f32_e32 v93, v93
	v_exp_f32_e32 v96, v96
	v_exp_f32_e32 v97, v97
	v_cvt_pk_fp8_f32 v130, v182, v183
	v_mfma_f32_32x32x64_f8f6f4 v[98:113], v[218:225], v[138:145], v[66:81]
	ds_read_b128 v[218:221], v198 offset:49152
	ds_read_b128 v[222:225], v199 offset:49152
	ds_read_b128 v[226:229], v198 offset:55296
	ds_read_b128 v[230:233], v199 offset:55296
	v_cvt_pk_fp8_f32 v134, v82, v83
	v_cvt_pk_fp8_f32 v131, v234, v235
	v_cvt_pk_fp8_f32 v135, v86, v87
	v_cvt_pk_fp8_f32 v132, v238, v239
	v_cvt_pk_fp8_f32 v136, v90, v91
	v_cvt_pk_fp8_f32 v133, v242, v243
	v_cvt_pk_fp8_f32 v137, v94, v95
	v_cvt_pk_fp8_f32 v130, v184, v185 op_sel:[0,0,1]
	v_cvt_pk_fp8_f32 v134, v84, v85 op_sel:[0,0,1]
	v_cvt_pk_fp8_f32 v131, v236, v237 op_sel:[0,0,1]
	v_cvt_pk_fp8_f32 v135, v88, v89 op_sel:[0,0,1]
	v_cvt_pk_fp8_f32 v132, v240, v241 op_sel:[0,0,1]
	v_cvt_pk_fp8_f32 v136, v92, v93 op_sel:[0,0,1]
	v_cvt_pk_fp8_f32 v133, v244, v245 op_sel:[0,0,1]
	s_waitcnt lgkmcnt(0)
	v_mfma_f32_32x32x64_f8f6f4 v[114:129], v[218:225], v[146:153], v[114:129]
	v_cvt_pk_fp8_f32 v137, v96, v97 op_sel:[0,0,1]
	v_mfma_f32_32x32x64_f8f6f4 v[98:113], v[226:233], v[146:153], v[98:113]
	ds_read_b128 v[218:221], v200 offset:49152
	ds_read_b128 v[222:225], v201 offset:49152
	ds_read_b128 v[226:229], v200 offset:55296
	ds_read_b128 v[230:233], v201 offset:55296
	s_waitcnt lgkmcnt(0)
	v_mfma_f32_32x32x64_f8f6f4 v[114:129], v[218:225], v[154:161], v[114:129]
	v_add_f32_e32 v218, 0, v182
	v_add_f32_e32 v218, v183, v218
	v_add_f32_e32 v218, v184, v218
	v_add_f32_e32 v218, v185, v218
	v_add_f32_e32 v218, v234, v218
	v_add_f32_e32 v218, v235, v218
	v_add_f32_e32 v218, v236, v218
	v_add_f32_e32 v218, v237, v218
	v_add_f32_e32 v218, v238, v218
	v_add_f32_e32 v218, v239, v218
	v_add_f32_e32 v218, v240, v218
	v_add_f32_e32 v218, v241, v218
	v_add_f32_e32 v218, v242, v218
	v_add_f32_e32 v218, v243, v218
	v_add_f32_e32 v218, v244, v218
	v_add_f32_e32 v218, v245, v218
	v_add_f32_e32 v218, v82, v218
	v_add_f32_e32 v218, v83, v218
	v_mfma_f32_32x32x64_f8f6f4 v[98:113], v[226:233], v[154:161], v[98:113]
	v_add_f32_e32 v218, v84, v218
	v_add_f32_e32 v218, v85, v218
	v_add_f32_e32 v218, v86, v218
	v_add_f32_e32 v218, v87, v218
	v_add_f32_e32 v218, v88, v218
	v_add_f32_e32 v218, v89, v218
	v_add_f32_e32 v218, v90, v218
	v_add_f32_e32 v218, v91, v218
	v_add_f32_e32 v218, v92, v218
	v_add_f32_e32 v218, v93, v218
	v_add_f32_e32 v218, v94, v218
	v_add_f32_e32 v218, v95, v218
	v_add_f32_e32 v218, v96, v218
	v_add_f32_e32 v218, v97, v218
	v_mov_b32_e32 v219, v218
	s_nop 1
	v_permlane32_swap_b32_e32 v218, v219
	s_cmp_eq_u32 s94, 0
	s_cbranch_scc0 .Lstg_mid4_l0
	s_waitcnt vmcnt(0)
	s_barrier
	s_mov_b32 m0, s92
	s_nop 0
	global_load_lds_dwordx4 v164, s[24:25]
	s_mov_b32 m0, s86
	s_nop 0
	global_load_lds_dwordx4 v170, s[26:27]
	s_add_u32 s24, s24, 0x3000
	s_addc_u32 s25, s25, 0
	s_add_u32 s26, s26, 64
	s_addc_u32 s27, s27, 0
.Lstg_mid4_l0:
	ds_read_b128 v[86:89], v194 offset:32768
	ds_read_b128 v[82:85], v193 offset:32768
	ds_read_b128 v[90:93], v193 offset:34816
	ds_read_b128 v[94:97], v194 offset:34816
	v_max_f32_e32 v182, v115, v115
	v_max_f32_e32 v183, v114, v114
	v_max_f32_e32 v182, v183, v182
	s_waitcnt lgkmcnt(0)
	v_mfma_f32_32x32x64_f8f6f4 v[2:17], v[130:137], v[82:89], v[2:17]
	v_max3_f32 v182, v182, v116, v117
	v_max3_f32 v182, v182, v118, v119
	v_max3_f32 v182, v182, v120, v121
	v_max3_f32 v182, v182, v122, v123
	v_max3_f32 v182, v182, v124, v125
	v_max3_f32 v182, v182, v126, v127
	v_max3_f32 v182, v182, v128, v129
	v_max3_f32 v182, v182, v98, v99
	v_mov_b32_e32 v220, 1.0
	v_mfma_f32_32x32x64_f8f6f4 v[50:65], v[130:137], v[90:97], v[50:65]
	ds_read_b128 v[82:85], v193 offset:36864
	ds_read_b128 v[90:93], v193 offset:38912
	ds_read_b128 v[86:89], v194 offset:36864
	ds_read_b128 v[94:97], v194 offset:38912
	s_waitcnt lgkmcnt(0)
	v_mfma_f32_32x32x64_f8f6f4 v[34:49], v[130:137], v[82:89], v[34:49]
	v_max3_f32 v82, v182, v100, v101
	v_max3_f32 v82, v82, v102, v103
	v_max3_f32 v82, v82, v104, v105
	v_max3_f32 v82, v82, v106, v107
	v_max3_f32 v82, v82, v108, v109
	v_max3_f32 v82, v82, v110, v111
	v_max3_f32 v82, v82, v112, v113
	v_mov_b32_e32 v83, v82
	s_nop 1
	v_permlane32_swap_b32_e32 v82, v83
	v_max_f32_e32 v83, v83, v83
	v_max_f32_e32 v82, v82, v82
	v_max_f32_e32 v82, v82, v83
	v_cmp_ge_f32_e32 vcc, s85, v82
	s_cmp_eq_u64 vcc, exec
	v_mfma_f32_32x32x64_f8f6f4 v[18:33], v[130:137], v[90:97], v[18:33]
	s_cbranch_scc0 .LBB0_935
	v_cmp_gt_f32_e32 vcc, 1.0, v220
	s_cbranch_vccz .LBB0_922

; __device__ __forceinline__ void finishSM(f32x16& p0, f32x16& p1, float alpha, float& l_reg, v8i& pa) {
; #pragma unroll
;   for (int r = 0; r < 16; ++r) p1[r] = __builtin_amdgcn_exp2f(p1[r]);
;   float ps = 0;
; #pragma unroll
;   for (int r = 0; r < 16; ++r) ps += p0[r];
; #pragma unroll
;   for (int r = 0; r < 16; ++r) ps += p1[r];
;   { auto rr = __builtin_amdgcn_permlane32_swap(__float_as_uint(ps), __float_as_uint(ps), false, false);
;     ps = __uint_as_float(rr[0]) + __uint_as_float(rr[1]); }
;   l_reg = l_reg * alpha + ps;
; #pragma unroll
;   for (int q = 0; q < 4; ++q) { int w0 = pa[q], w1 = pa[4 + q];
;     w0 = __builtin_amdgcn_cvt_pk_fp8_f32(p0[4 * q], p0[4 * q + 1], w0, false); w0 = __builtin_amdgcn_cvt_pk_fp8_f32(p0[4 * q + 2], p0[4 * q + 3], w0, true);
;     w1 = __builtin_amdgcn_cvt_pk_fp8_f32(p1[4 * q], p1[4 * q + 1], w1, false); w1 = __builtin_amdgcn_cvt_pk_fp8_f32(p1[4 * q + 2], p1[4 * q + 3], w1, true);
;     pa[q] = w0; pa[4 + q] = w1; }
; }
; __device__ __forceinline__ void qkt(f32x16& p0, f32x16& p1, const char* Ks, const v8i* qr, int r32, int hi, const f32x16& nm16) {
; #pragma unroll
;   for (int s = 0; s < 3; ++s) { const int c0 = 4 * s + 2 * hi;
;     const v8i a0 = __builtin_shufflevector(*reinterpret_cast<const v4i*>(Ks + k8_off(r32, c0)), *reinterpret_cast<const v4i*>(Ks + k8_off(r32, c0 + 1)), 0, 1, 2, 3, 4, 5, 6, 7);
;     const v8i a1 = __builtin_shufflevector(*reinterpret_cast<const v4i*>(Ks + 32 * DQK + k8_off(r32, c0)), *reinterpret_cast<const v4i*>(Ks + 32 * DQK + k8_off(r32, c0 + 1)), 0, 1, 2, 3, 4, 5, 6, 7);
;     p0 = __builtin_amdgcn_mfma_scale_f32_32x32x64_f8f6f4(a0, qr[s], s == 0 ? nm16 : p0, 0, 0, 0, 0, 0, 0);
;     p1 = __builtin_amdgcn_mfma_scale_f32_32x32x64_f8f6f4(a1, qr[s], s == 0 ? nm16 : p1, 0, 0, 0, 0, 0, 0); }
; }
; __device__ __forceinline__ void pv_d0(f32x16* o, const char* Vs, v8i pa, int r32, int hi) {
; #pragma unroll
;   for (int d0 = 0; d0 < 4; ++d0) { const int row = 32 * d0 + r32, x = (row >> 2) & 3;
;     const v8i vb = __builtin_shufflevector(*reinterpret_cast<const v4i*>(Vs + row * 64 + (((2 * hi) ^ x) << 4)), *reinterpret_cast<const v4i*>(Vs + row * 64 + (((2 * hi + 1) ^ x) << 4)), 0, 1, 2, 3, 4, 5, 6, 7);
;     o[d0] = __builtin_amdgcn_mfma_scale_f32_32x32x64_f8f6f4(pa, vb, o[d0], 0, 0, 0, 0, 0, 0); }
; }
.Lstg_end4_l0:
	v_exp_f32_e32 v176, v114
	v_exp_f32_e32 v177, v115
	v_exp_f32_e32 v178, v116
	v_exp_f32_e32 v179, v117
	v_exp_f32_e32 v180, v118
	v_exp_f32_e32 v181, v119
	v_exp_f32_e32 v182, v120
	v_exp_f32_e32 v183, v121
	v_exp_f32_e32 v184, v122
	v_exp_f32_e32 v185, v123
	v_exp_f32_e32 v221, v124
	v_exp_f32_e32 v238, v125
	v_exp_f32_e32 v239, v126
	v_exp_f32_e32 v240, v127
	v_exp_f32_e32 v241, v128
	v_exp_f32_e32 v242, v129
	ds_read_b128 v[82:85], v196 offset:8192
	ds_read_b128 v[86:89], v197 offset:8192
	ds_read_b128 v[222:225], v196 offset:14336
	ds_read_b128 v[226:229], v197 offset:14336
	v_exp_f32_e32 v100, v100
	v_exp_f32_e32 v101, v101
	s_waitcnt lgkmcnt(0)
	v_mfma_f32_32x32x64_f8f6f4 v[114:129], v[82:89], v[138:145], v[66:81]
	v_exp_f32_e32 v102, v102
	v_exp_f32_e32 v103, v103
	v_exp_f32_e32 v104, v104
	v_exp_f32_e32 v105, v105
	v_exp_f32_e32 v106, v106
	v_exp_f32_e32 v107, v107
	v_exp_f32_e32 v108, v108
	v_exp_f32_e32 v110, v110
	v_exp_f32_e32 v111, v111
	v_exp_f32_e32 v109, v109
	v_exp_f32_e32 v112, v112
	v_exp_f32_e32 v113, v113
	v_cvt_pk_fp8_f32 v130, v176, v177
	v_cvt_pk_fp8_f32 v131, v180, v181
	v_cvt_pk_fp8_f32 v135, v102, v103
	v_mfma_f32_32x32x64_f8f6f4 v[82:97], v[222:229], v[138:145], v[66:81]
	ds_read_b128 v[222:225], v198 offset:8192
	ds_read_b128 v[226:229], v199 offset:8192
	ds_read_b128 v[230:233], v198 offset:14336
	ds_read_b128 v[234:237], v199 offset:14336
	v_cvt_pk_fp8_f32 v132, v184, v185
	v_cvt_pk_fp8_f32 v136, v106, v107
	v_cvt_pk_fp8_f32 v133, v239, v240
	v_cvt_pk_fp8_f32 v137, v110, v111
	v_cvt_pk_fp8_f32 v130, v178, v179 op_sel:[0,0,1]
	v_cvt_pk_fp8_f32 v131, v182, v183 op_sel:[0,0,1]
	v_cvt_pk_fp8_f32 v135, v104, v105 op_sel:[0,0,1]
	v_cvt_pk_fp8_f32 v132, v221, v238 op_sel:[0,0,1]
	v_cvt_pk_fp8_f32 v136, v108, v109 op_sel:[0,0,1]
	v_cvt_pk_fp8_f32 v133, v241, v242 op_sel:[0,0,1]
	v_cvt_pk_fp8_f32 v137, v112, v113 op_sel:[0,0,1]
	s_waitcnt lgkmcnt(0)
	v_mfma_f32_32x32x64_f8f6f4 v[114:129], v[222:229], v[146:153], v[114:129]
	v_mfma_f32_32x32x64_f8f6f4 v[82:97], v[230:237], v[146:153], v[82:97]
	ds_read_b128 v[222:225], v200 offset:8192
	ds_read_b128 v[226:229], v201 offset:8192
	ds_read_b128 v[230:233], v200 offset:14336
	ds_read_b128 v[234:237], v201 offset:14336
	s_waitcnt lgkmcnt(0)
	v_mfma_f32_32x32x64_f8f6f4 v[114:129], v[222:229], v[154:161], v[114:129]
	v_exp_f32_e32 v222, v98
	v_add_f32_e32 v98, 0, v176
	v_add_f32_e32 v98, v177, v98
	v_add_f32_e32 v98, v178, v98
	v_add_f32_e32 v98, v179, v98
	v_add_f32_e32 v98, v180, v98
	v_add_f32_e32 v98, v181, v98
	v_add_f32_e32 v98, v182, v98
	v_add_f32_e32 v98, v183, v98
	v_add_f32_e32 v98, v184, v98
	v_add_f32_e32 v98, v185, v98
	v_add_f32_e32 v98, v221, v98
	v_add_f32_e32 v98, v238, v98
	v_add_f32_e32 v98, v239, v98
	v_exp_f32_e32 v223, v99
	v_add_f32_e32 v98, v240, v98
	v_add_f32_e32 v98, v241, v98
	v_add_f32_e32 v98, v242, v98
	v_add_f32_e32 v98, v222, v98
	v_add_f32_e32 v98, v223, v98
	v_mfma_f32_32x32x64_f8f6f4 v[82:97], v[230:237], v[154:161], v[82:97]
	v_add_f32_e32 v98, v100, v98
	v_add_f32_e32 v98, v101, v98
	v_add_f32_e32 v98, v102, v98
	v_add_f32_e32 v98, v103, v98
	v_add_f32_e32 v98, v104, v98
	v_add_f32_e32 v98, v105, v98
	v_add_f32_e32 v98, v106, v98
	v_add_f32_e32 v98, v107, v98
	v_add_f32_e32 v98, v108, v98
	v_cvt_pk_fp8_f32 v134, v222, v223
	v_add_f32_e32 v98, v109, v98
	v_add_f32_e32 v98, v110, v98
	v_add_f32_e32 v98, v111, v98
	v_add_f32_e32 v98, v112, v98
	v_cvt_pk_fp8_f32 v134, v100, v101 op_sel:[0,0,1]
	v_add_f32_e32 v98, v113, v98
	v_mov_b32_e32 v99, v98
	s_nop 1
	v_permlane32_swap_b32_e32 v98, v99
	s_cmp_eq_u32 s94, 0
	s_cbranch_scc0 .Lstg_mid5_l0
	s_waitcnt vmcnt(0)
	s_barrier
	s_cmp_lt_i32 s9, 49
	s_cbranch_scc0 .Lstg_mid5_l0
	s_mov_b32 m0, s90
	s_nop 0
	global_load_lds_dwordx4 v164, s[24:25]
	s_mov_b32 m0, s88
	s_nop 0
	global_load_lds_dwordx4 v170, s[26:27]
	s_add_u32 s24, s24, 0x3000
	s_addc_u32 s25, s25, 0
	s_add_u32 s26, s26, 64
	s_addc_u32 s27, s27, 0
.Lstg_mid5_l0:
	ds_read_b128 v[104:107], v194 offset:40960
	ds_read_b128 v[100:103], v193 offset:40960
	ds_read_b128 v[222:225], v193 offset:43008
	ds_read_b128 v[226:229], v194 offset:43008
	v_max_f32_e32 v108, v115, v115
	v_max_f32_e32 v109, v114, v114
	v_max_f32_e32 v108, v109, v108
	s_waitcnt lgkmcnt(0)
	v_mfma_f32_32x32x64_f8f6f4 v[2:17], v[130:137], v[100:107], v[2:17]
	v_max3_f32 v108, v108, v116, v117
	v_max3_f32 v108, v108, v118, v119
	v_max3_f32 v108, v108, v120, v121
	v_max3_f32 v108, v108, v122, v123
	v_max3_f32 v108, v108, v124, v125
	v_max3_f32 v108, v108, v126, v127
	v_max3_f32 v108, v108, v128, v129
	v_max3_f32 v108, v108, v82, v83
	v_mov_b32_e32 v176, 1.0
	v_mfma_f32_32x32x64_f8f6f4 v[50:65], v[130:137], v[222:229], v[50:65]
	ds_read_b128 v[100:103], v193 offset:45056
	ds_read_b128 v[222:225], v193 offset:47104
	ds_read_b128 v[104:107], v194 offset:45056
	ds_read_b128 v[226:229], v194 offset:47104
	s_waitcnt lgkmcnt(0)
	v_mfma_f32_32x32x64_f8f6f4 v[34:49], v[130:137], v[100:107], v[34:49]
	v_max3_f32 v100, v108, v84, v85
	v_max3_f32 v100, v100, v86, v87
	v_max3_f32 v100, v100, v88, v89
	v_max3_f32 v100, v100, v90, v91
	v_max3_f32 v100, v100, v92, v93
	v_max3_f32 v100, v100, v94, v95
	v_max3_f32 v100, v100, v96, v97
	v_mov_b32_e32 v101, v100
	s_nop 1
	v_permlane32_swap_b32_e32 v100, v101
	v_max_f32_e32 v101, v101, v101
	v_max_f32_e32 v100, v100, v100
	v_max_f32_e32 v100, v100, v101
	v_cmp_ge_f32_e32 vcc, s85, v100
	s_cmp_eq_u64 vcc, exec
	v_mfma_f32_32x32x64_f8f6f4 v[18:33], v[130:137], v[222:229], v[18:33]
	s_cbranch_scc0 .LBB0_936
	v_cmp_gt_f32_e32 vcc, 1.0, v176
	s_cbranch_vccz .LBB0_929

; #define ASTEP_B(jt, bp, bc, bn) ASTEP(pB0, pB1, alB, pA0, pA1, alA, jt, bp, bc, bn)
; #define ASTEP_A(jt, bp, bc, bn) ASTEP(pA0, pA1, alA, pB0, pB1, alB, jt, bp, bc, bn)
; __device__ __forceinline__ void finishSM(f32x16& p0, f32x16& p1, float alpha, float& l_reg, v8i& pa) {
; #pragma unroll
;   for (int r = 0; r < 16; ++r) p1[r] = __builtin_amdgcn_exp2f(p1[r]);
;   float ps = 0;
; #pragma unroll
;   for (int r = 0; r < 16; ++r) ps += p0[r];
; #pragma unroll
;   for (int r = 0; r < 16; ++r) ps += p1[r];
;   { auto rr = __builtin_amdgcn_permlane32_swap(__float_as_uint(ps), __float_as_uint(ps), false, false);
;     ps = __uint_as_float(rr[0]) + __uint_as_float(rr[1]); }
;   l_reg = l_reg * alpha + ps;
; #pragma unroll
;   for (int q = 0; q < 4; ++q) { int w0 = pa[q], w1 = pa[4 + q];
;     w0 = __builtin_amdgcn_cvt_pk_fp8_f32(p0[4 * q], p0[4 * q + 1], w0, false); w0 = __builtin_amdgcn_cvt_pk_fp8_f32(p0[4 * q + 2], p0[4 * q + 3], w0, true);
;     w1 = __builtin_amdgcn_cvt_pk_fp8_f32(p1[4 * q], p1[4 * q + 1], w1, false); w1 = __builtin_amdgcn_cvt_pk_fp8_f32(p1[4 * q + 2], p1[4 * q + 3], w1, true);
;     pa[q] = w0; pa[4 + q] = w1; }
; }
; __device__ __forceinline__ void attn_unit(const unsigned char* __restrict__ CQt, const unsigned char* __restrict__ Wh, const f32x2* __restrict__ cst, const unsigned char* __restrict__ Kh, const unsigned char* __restrict__ Vh, bf16* __restrict__ Ob, char* lds) {
;     ...
; #pragma nounroll
;   for (int j = 1; j <= 55; j += 6) {
;     ASTEP_B(j, 0, 1, 2); ASTEP_A(j + 1, 1, 2, 0); ASTEP_B(j + 2, 2, 0, 1);
;     ASTEP_A(j + 3, 0, 1, 2); ASTEP_B(j + 4, 1, 2, 0); ASTEP_A(j + 5, 2, 0, 1);
;   }
.LBB0_929:
	v_add_f32_e32 v100, v206, v207
	v_fmac_f32_e32 v100, v205, v162
	v_add_f32_e32 v101, v209, v210
	v_fmac_f32_e32 v101, v100, v208
	v_add_f32_e32 v100, v212, v213
	v_exp_f32_e32 v235, v114
	v_exp_f32_e32 v236, v115
	v_exp_f32_e32 v233, v116
	v_exp_f32_e32 v234, v117
	v_exp_f32_e32 v231, v118
	v_exp_f32_e32 v232, v119
	v_exp_f32_e32 v229, v120
	v_exp_f32_e32 v230, v121
	v_exp_f32_e32 v227, v122
	v_exp_f32_e32 v228, v123
	v_exp_f32_e32 v225, v124
	v_exp_f32_e32 v226, v125
	v_exp_f32_e32 v223, v126
	v_exp_f32_e32 v224, v127
	v_exp_f32_e32 v221, v128
	v_exp_f32_e32 v222, v129
	v_fmac_f32_e32 v100, v101, v211
	v_add_f32_e32 v101, v215, v216
	v_fmac_f32_e32 v101, v100, v214
	v_add_f32_e32 v100, v218, v219
	s_cmp_eq_u32 s94, 0
	s_cbranch_scc1 .Lstg_end5_l0
	s_waitcnt vmcnt(0)
	s_barrier
.Lstg_end5_l0:
	v_fmac_f32_e32 v100, v101, v217
	v_add_f32_e32 v162, v98, v99
	s_add_i32 s9, s9, 6
	v_fmac_f32_e32 v162, v100, v220
	s_cmp_gt_u32 s9, 49
	s_cbranch_scc1 .LBB0_937
	v_mov_b32_e32 v205, v176
	s_branch .LBB0_887

; __device__ __forceinline__ void qkt(f32x16& p0, f32x16& p1, const char* Ks, const v8i* qr, int r32, int hi, const f32x16& nm16) {
; #pragma unroll
;   for (int s = 0; s < 3; ++s) { const int c0 = 4 * s + 2 * hi;
;     const v8i a0 = __builtin_shufflevector(*reinterpret_cast<const v4i*>(Ks + k8_off(r32, c0)), *reinterpret_cast<const v4i*>(Ks + k8_off(r32, c0 + 1)), 0, 1, 2, 3, 4, 5, 6, 7);
;     const v8i a1 = __builtin_shufflevector(*reinterpret_cast<const v4i*>(Ks + 32 * DQK + k8_off(r32, c0)), *reinterpret_cast<const v4i*>(Ks + 32 * DQK + k8_off(r32, c0 + 1)), 0, 1, 2, 3, 4, 5, 6, 7);
;     p0 = __builtin_amdgcn_mfma_scale_f32_32x32x64_f8f6f4(a0, qr[s], s == 0 ? nm16 : p0, 0, 0, 0, 0, 0, 0);
;     p1 = __builtin_amdgcn_mfma_scale_f32_32x32x64_f8f6f4(a1, qr[s], s == 0 ? nm16 : p1, 0, 0, 0, 0, 0, 0); }
; }
; __device__ __forceinline__ void pv_d0(f32x16* o, const char* Vs, v8i pa, int r32, int hi) {
; #pragma unroll
;   for (int d0 = 0; d0 < 4; ++d0) { const int row = 32 * d0 + r32, x = (row >> 2) & 3;
;     const v8i vb = __builtin_shufflevector(*reinterpret_cast<const v4i*>(Vs + row * 64 + (((2 * hi) ^ x) << 4)), *reinterpret_cast<const v4i*>(Vs + row * 64 + (((2 * hi + 1) ^ x) << 4)), 0, 1, 2, 3, 4, 5, 6, 7);
;     o[d0] = __builtin_amdgcn_mfma_scale_f32_32x32x64_f8f6f4(pa, vb, o[d0], 0, 0, 0, 0, 0, 0); }
; }
; __device__ __forceinline__ void attn_unit(const unsigned char* __restrict__ CQt, const unsigned char* __restrict__ Wh, const f32x2* __restrict__ cst, const unsigned char* __restrict__ Kh, const unsigned char* __restrict__ Vh, bf16* __restrict__ Ob, char* lds) {
;   int tid = threadIdx.x; asm volatile("" : "+v"(tid));
;   const int wid = __builtin_amdgcn_readfirstlane(tid >> 6), lane = tid & 63, r32 = lane & 31, hi = lane >> 5;
;     ...
;   constexpr int WIMG = 32 * 1024;
;   float* wsp = (float*)(lds + 60 * 1024) + wid * 64; float* li_l = wsp; float* al_l = wsp + 32;
;   float m_reg = 0.f, l_reg = 0; f32x16 o[4] = {}; v8i qr[3]; f32x16 nm16 = {};
;   int koff[2], voff[2];
; #pragma unroll
;   for (int i = 0; i < 2; ++i) { const int m = (i * 8 + wid) * 64 + lane, row = m / 12, cp = m % 12; const int c = (cp & ~3) | ((cp & 3) ^ ((row >> 2) & 3)); koff[i] = row * DQK + c * 16; }
;   { const int m = wid * 64 + lane, d = m >> 2, cp = m & 3; voff[0] = d * SEQ + ((cp ^ ((d >> 2) & 3)) << 4); voff[1] = 0; }
.LBB0_937:
	s_barrier
	s_add_u32 s10, s0, 0xba000
	s_addc_u32 s11, s1, 0
	s_mov_b32 m0, s90
	v_lshl_add_u64 v[98:99], s[10:11], 0, v[164:165]
	global_load_lds_dwordx4 v[98:99], off
	s_and_b64 vcc, exec, s[64:65]
	s_cbranch_vccz .LBB0_939
	v_lshl_add_u64 v[98:99], s[10:11], 0, v[166:167]
	s_mov_b32 m0, s91
	s_nop 0
	global_load_lds_dwordx4 v[98:99], off
.LBB0_939:
	v_lshl_add_u64 v[98:99], v[168:169], 0, s[56:57]
	s_mov_b32 m0, s89
	s_nop 0
	global_load_lds_dwordx4 v[98:99], off
	s_mov_b32 m0, s88
	s_nop 0
	global_load_lds_dwordx4 v170, s[26:27]
	ds_read_b128 v[102:105], v197 offset:20480
	ds_read_b128 v[98:101], v196 offset:20480
	ds_read_b128 v[202:205], v196 offset:26624
	ds_read_b128 v[206:209], v197 offset:26624
	v_add_f32_e32 v170, 0, v235
	ds_read_b128 v[210:213], v198 offset:20480
	ds_read_b128 v[238:241], v198 offset:26624
	ds_read_b128 v[214:217], v199 offset:20480
	ds_read_b128 v[242:245], v199 offset:26624
	ds_read_b128 v[246:249], v200 offset:20480
	ds_read_b128 v[178:181], v200 offset:26624
	ds_read_b128 v[250:253], v201 offset:20480
	ds_read_b128 v[182:185], v201 offset:26624
	s_waitcnt lgkmcnt(0)
	v_mfma_f32_32x32x64_f8f6f4 v[114:129], v[98:105], v[138:145], v[66:81]
	v_add_f32_e32 v170, v236, v170
	v_add_f32_e32 v170, v233, v170
	v_add_f32_e32 v170, v234, v170
	v_add_f32_e32 v170, v231, v170
	v_add_f32_e32 v170, v232, v170
	v_add_f32_e32 v170, v229, v170
	v_add_f32_e32 v170, v230, v170
	v_add_f32_e32 v170, v227, v170
	v_add_f32_e32 v170, v228, v170
	v_add_f32_e32 v170, v225, v170
	v_add_f32_e32 v170, v226, v170
	v_exp_f32_e32 v82, v82
	v_add_f32_e32 v170, v223, v170
	v_exp_f32_e32 v83, v83
	v_add_f32_e32 v170, v224, v170
	v_mfma_f32_32x32x64_f8f6f4 v[98:113], v[202:209], v[138:145], v[66:81]
	v_exp_f32_e32 v84, v84
	v_add_f32_e32 v170, v221, v170
	v_exp_f32_e32 v85, v85
	v_add_f32_e32 v170, v222, v170
	v_exp_f32_e32 v86, v86
	v_add_f32_e32 v170, v82, v170
	v_exp_f32_e32 v87, v87
	v_add_f32_e32 v170, v83, v170
	v_exp_f32_e32 v88, v88
	v_add_f32_e32 v170, v84, v170
	v_exp_f32_e32 v89, v89
	v_add_f32_e32 v170, v85, v170
	v_exp_f32_e32 v90, v90
	v_add_f32_e32 v170, v86, v170
	v_exp_f32_e32 v91, v91
	v_mfma_f32_32x32x64_f8f6f4 v[114:129], v[210:217], v[146:153], v[114:129]
	v_add_f32_e32 v170, v87, v170
	v_exp_f32_e32 v92, v92
	v_exp_f32_e32 v94, v94
	v_exp_f32_e32 v95, v95
	v_add_f32_e32 v170, v88, v170
	v_exp_f32_e32 v93, v93
	v_add_f32_e32 v170, v89, v170
	v_add_f32_e32 v170, v90, v170
	v_add_f32_e32 v170, v91, v170
	v_exp_f32_e32 v96, v96
	v_exp_f32_e32 v97, v97
	v_add_f32_e32 v170, v92, v170
	v_cvt_pk_fp8_f32 v130, v235, v236
	v_cvt_pk_fp8_f32 v134, v82, v83
	v_cvt_pk_fp8_f32 v131, v231, v232
	v_mfma_f32_32x32x64_f8f6f4 v[98:113], v[238:245], v[146:153], v[98:113]
	v_cvt_pk_fp8_f32 v135, v86, v87
	v_cvt_pk_fp8_f32 v132, v227, v228
	v_cvt_pk_fp8_f32 v136, v90, v91
	v_cvt_pk_fp8_f32 v133, v223, v224
	v_cvt_pk_fp8_f32 v137, v94, v95
	v_add_f32_e32 v170, v93, v170
	v_add_f32_e32 v170, v94, v170
	v_add_f32_e32 v170, v95, v170
	v_add_f32_e32 v170, v96, v170
	v_cvt_pk_fp8_f32 v130, v233, v234 op_sel:[0,0,1]
	v_cvt_pk_fp8_f32 v134, v84, v85 op_sel:[0,0,1]
	v_cvt_pk_fp8_f32 v131, v229, v230 op_sel:[0,0,1]
	v_cvt_pk_fp8_f32 v135, v88, v89 op_sel:[0,0,1]
	v_cvt_pk_fp8_f32 v132, v225, v226 op_sel:[0,0,1]
	v_cvt_pk_fp8_f32 v136, v92, v93 op_sel:[0,0,1]
	v_mfma_f32_32x32x64_f8f6f4 v[114:129], v[246:253], v[154:161], v[114:129]
	v_cvt_pk_fp8_f32 v133, v221, v222 op_sel:[0,0,1]
	v_cvt_pk_fp8_f32 v137, v96, v97 op_sel:[0,0,1]
	v_add_f32_e32 v170, v97, v170
	v_mov_b32_e32 v171, v170
	s_nop 1
	v_permlane32_swap_b32_e32 v170, v171
	v_mfma_f32_32x32x64_f8f6f4 v[98:113], v[178:185], v[154:161], v[98:113]
	ds_read_b128 v[86:89], v194
	ds_read_b128 v[82:85], v193
	ds_read_b128 v[90:93], v193 offset:2048
	ds_read_b128 v[94:97], v194 offset:2048
	s_nop 7
	v_max_f32_e32 v172, v115, v115
	v_max_f32_e32 v173, v114, v114
	v_max_f32_e32 v172, v173, v172
	s_waitcnt lgkmcnt(0)
	v_mfma_f32_32x32x64_f8f6f4 v[2:17], v[130:137], v[82:89], v[2:17]
	v_max3_f32 v172, v172, v116, v117
	v_max3_f32 v172, v172, v118, v119
	v_max3_f32 v172, v172, v120, v121
	v_max3_f32 v172, v172, v122, v123
	v_max3_f32 v172, v172, v124, v125
	v_max3_f32 v172, v172, v126, v127
	v_max3_f32 v172, v172, v128, v129
	v_max3_f32 v172, v172, v98, v99
	v_mfma_f32_32x32x64_f8f6f4 v[50:65], v[130:137], v[90:97], v[50:65]
	ds_read_b128 v[82:85], v193 offset:4096
	ds_read_b128 v[90:93], v193 offset:6144
	ds_read_b128 v[86:89], v194 offset:4096
	ds_read_b128 v[94:97], v194 offset:6144
	s_waitcnt lgkmcnt(0)
	v_mfma_f32_32x32x64_f8f6f4 v[34:49], v[130:137], v[82:89], v[34:49]
	v_max3_f32 v82, v172, v100, v101
	v_max3_f32 v82, v82, v102, v103
	v_max3_f32 v82, v82, v104, v105
	v_max3_f32 v82, v82, v106, v107
	v_max3_f32 v82, v82, v108, v109
	v_max3_f32 v82, v82, v110, v111
	v_max3_f32 v82, v82, v112, v113
	v_mov_b32_e32 v83, v82
	s_nop 1
	v_permlane32_swap_b32_e32 v82, v83
	v_max_f32_e32 v83, v83, v83
	v_max_f32_e32 v82, v82, v82
	v_max_f32_e32 v82, v82, v83
	v_cmp_ge_f32_e32 vcc, s85, v82
	s_cmp_eq_u64 vcc, exec
	v_mfma_f32_32x32x64_f8f6f4 v[18:33], v[130:137], v[90:97], v[18:33]
	v_mov_b32_e32 v172, 1.0
	s_cbranch_scc0 .LBB0_1086
	v_cmp_gt_f32_e32 vcc, 1.0, v172
	s_cbranch_vccz .LBB0_944

; __device__ __forceinline__ void attn_unit(const unsigned char* __restrict__ CQt, const unsigned char* __restrict__ Wh, const f32x2* __restrict__ cst, const unsigned char* __restrict__ Kh, const unsigned char* __restrict__ Vh, bf16* __restrict__ Ob, char* lds) {
;     ...
;       if (s3 == 2) {
; #pragma unroll
;         for (int r = 0; r < 16; r += 2) { const f32x2 c0 = cc[r >> 1], c1 = cc[8 + (r >> 1)];
;           const float x0 = a0[r], y0 = a0[r + 1], x1 = a1[r], y1 = a1[r + 1];
;           a0[r] = x0 * c0.x - y0 * c0.y; a0[r + 1] = y0 * c0.x + x0 * c0.y; a1[r] = x1 * c1.x - y1 * c1.y; a1[r + 1] = y1 * c1.x + x1 * c1.y; } }
; #pragma unroll
;       for (int q = 0; q < 4; ++q) { int u0 = 0, u1 = 0;
;         u0 = __builtin_amdgcn_cvt_pk_fp8_f32(a0[4 * q] * QS, a0[4 * q + 1] * QS, u0, false); u0 = __builtin_amdgcn_cvt_pk_fp8_f32(a0[4 * q + 2] * QS, a0[4 * q + 3] * QS, u0, true);
;         u1 = __builtin_amdgcn_cvt_pk_fp8_f32(a1[4 * q] * QS, a1[4 * q + 1] * QS, u1, false); u1 = __builtin_amdgcn_cvt_pk_fp8_f32(a1[4 * q + 2] * QS, a1[4 * q + 3] * QS, u1, true);
;         qr[s3][q] = u0; qr[s3][4 + q] = u1; }
.LBB0_2149:
	v_mul_f32_e32 v2, 0x3c553b94, v2
	v_mul_f32_e32 v3, 0x3c553b94, v3
	v_mov_b32_e32 v142, 0
	v_cvt_pk_fp8_f32 v142, v2, v3
	v_mul_f32_e32 v2, 0x3c553b94, v4
	v_mul_f32_e32 v3, 0x3c553b94, v5
	v_mov_b32_e32 v139, 0
	v_cvt_pk_fp8_f32 v142, v2, v3 op_sel:[0,0,1]
	v_mul_f32_e32 v2, 0x3c553b94, v22
	v_mul_f32_e32 v3, 0x3c553b94, v23
	v_cvt_pk_fp8_f32 v139, v2, v3
	v_mul_f32_e32 v4, 0x3c553b94, v6
	v_mul_f32_e32 v5, 0x3c553b94, v7
	v_mov_b32_e32 v143, 0
	v_cvt_pk_fp8_f32 v143, v4, v5
	v_mul_f32_e32 v2, 0x3c553b94, v24
	v_mul_f32_e32 v3, 0x3c553b94, v25
	v_cvt_pk_fp8_f32 v139, v2, v3 op_sel:[0,0,1]
	v_mul_f32_e32 v2, 0x3c553b94, v8
	v_mul_f32_e32 v3, 0x3c553b94, v9
	v_cvt_pk_fp8_f32 v143, v2, v3 op_sel:[0,0,1]
	v_mul_f32_e32 v2, 0x3c553b94, v26
	v_mul_f32_e32 v3, 0x3c553b94, v27
	v_mov_b32_e32 v140, 0
	v_cvt_pk_fp8_f32 v140, v2, v3
	v_mul_f32_e32 v4, 0x3c553b94, v10
	v_mul_f32_e32 v5, 0x3c553b94, v11
	v_mov_b32_e32 v144, 0
	v_cvt_pk_fp8_f32 v144, v4, v5
	v_mul_f32_e32 v2, 0x3c553b94, v28
	v_mul_f32_e32 v3, 0x3c553b94, v29
	v_cvt_pk_fp8_f32 v140, v2, v3 op_sel:[0,0,1]
	v_mul_f32_e32 v2, 0x3c553b94, v12
	v_mul_f32_e32 v3, 0x3c553b94, v13
	v_cvt_pk_fp8_f32 v144, v2, v3 op_sel:[0,0,1]
	v_mul_f32_e32 v2, 0x3c553b94, v30
	v_mul_f32_e32 v3, 0x3c553b94, v31
	v_mov_b32_e32 v141, 0
	v_cvt_pk_fp8_f32 v141, v2, v3
	v_mul_f32_e32 v4, 0x3c553b94, v14
	v_mul_f32_e32 v5, 0x3c553b94, v15
	v_mov_b32_e32 v145, 0
	v_cvt_pk_fp8_f32 v145, v4, v5
	v_mul_f32_e32 v2, 0x3c553b94, v32
	v_mul_f32_e32 v3, 0x3c553b94, v33
	v_cvt_pk_fp8_f32 v141, v2, v3 op_sel:[0,0,1]
	v_mul_f32_e32 v2, 0x3c553b94, v16
	v_mul_f32_e32 v3, 0x3c553b94, v17
	v_cvt_pk_fp8_f32 v145, v2, v3 op_sel:[0,0,1]
	v_mul_f32_e32 v2, 0x3c553b94, v50
	v_mul_f32_e32 v3, 0x3c553b94, v51
	v_mov_b32_e32 v146, 0
	v_cvt_pk_fp8_f32 v146, v2, v3
	v_mul_f32_e32 v4, 0x3c553b94, v34
	v_mul_f32_e32 v5, 0x3c553b94, v35
	v_mov_b32_e32 v150, 0
	v_cvt_pk_fp8_f32 v150, v4, v5
	v_mul_f32_e32 v2, 0x3c553b94, v52
	v_mul_f32_e32 v3, 0x3c553b94, v53
	v_cvt_pk_fp8_f32 v146, v2, v3 op_sel:[0,0,1]
	v_mul_f32_e32 v2, 0x3c553b94, v36
	v_mul_f32_e32 v3, 0x3c553b94, v37
	v_cvt_pk_fp8_f32 v150, v2, v3 op_sel:[0,0,1]
	v_mul_f32_e32 v2, 0x3c553b94, v54
	v_mul_f32_e32 v3, 0x3c553b94, v55
	v_mov_b32_e32 v147, 0
	v_cvt_pk_fp8_f32 v147, v2, v3
	v_mul_f32_e32 v4, 0x3c553b94, v38
	v_mul_f32_e32 v5, 0x3c553b94, v39
	v_mov_b32_e32 v151, 0
	v_cvt_pk_fp8_f32 v151, v4, v5
	v_mul_f32_e32 v2, 0x3c553b94, v56
	v_mul_f32_e32 v3, 0x3c553b94, v57
	v_cvt_pk_fp8_f32 v147, v2, v3 op_sel:[0,0,1]
	v_mul_f32_e32 v2, 0x3c553b94, v40
	v_mul_f32_e32 v3, 0x3c553b94, v41
	v_cvt_pk_fp8_f32 v151, v2, v3 op_sel:[0,0,1]
	v_mul_f32_e32 v2, 0x3c553b94, v58
	v_mul_f32_e32 v3, 0x3c553b94, v59
	v_mov_b32_e32 v148, 0
	v_cvt_pk_fp8_f32 v148, v2, v3
	v_mul_f32_e32 v4, 0x3c553b94, v42
	v_mul_f32_e32 v5, 0x3c553b94, v43
	v_mov_b32_e32 v152, 0
	v_cvt_pk_fp8_f32 v152, v4, v5
	v_mul_f32_e32 v2, 0x3c553b94, v60
	v_mul_f32_e32 v3, 0x3c553b94, v61
	v_cvt_pk_fp8_f32 v148, v2, v3 op_sel:[0,0,1]
	v_mul_f32_e32 v2, 0x3c553b94, v44
	v_mul_f32_e32 v3, 0x3c553b94, v45
	v_cvt_pk_fp8_f32 v152, v2, v3 op_sel:[0,0,1]
	v_mul_f32_e32 v2, 0x3c553b94, v62
	v_mul_f32_e32 v3, 0x3c553b94, v63
	v_mov_b32_e32 v149, 0
	v_cvt_pk_fp8_f32 v149, v2, v3
	v_mul_f32_e32 v4, 0x3c553b94, v46
	v_mul_f32_e32 v5, 0x3c553b94, v47
	v_mov_b32_e32 v153, 0
	v_cvt_pk_fp8_f32 v153, v4, v5
	v_mul_f32_e32 v2, 0x3c553b94, v64
	v_mul_f32_e32 v3, 0x3c553b94, v65
	v_cvt_pk_fp8_f32 v149, v2, v3 op_sel:[0,0,1]
	v_mul_f32_e32 v2, 0x3c553b94, v48
	v_mul_f32_e32 v3, 0x3c553b94, v49
	v_cvt_pk_fp8_f32 v153, v2, v3 op_sel:[0,0,1]
	s_waitcnt vmcnt(0)
	v_pk_mul_f32 v[2:3], v[134:135], v[82:83]
	v_mov_b32_e32 v154, 0
	v_sub_f32_e32 v4, v2, v3
	v_pk_mul_f32 v[2:3], v[134:135], v[82:83] op_sel:[0,1] op_sel_hi:[1,0]
	v_mov_b32_e32 v158, 0
	v_add_f32_e32 v5, v2, v3
	v_pk_mul_f32 v[2:3], v[136:137], v[84:85]
	s_mov_b32 m0, s88
	v_sub_f32_e32 v10, v2, v3
	v_pk_mul_f32 v[2:3], v[136:137], v[84:85] op_sel:[0,1] op_sel_hi:[1,0]
	v_or_b32_e32 v99, 1, v156
	v_add_f32_e32 v11, v2, v3
	v_pk_mul_f32 v[2:3], v[130:131], v[86:87]
	v_lshrrev_b32_e32 v65, 2, v189
	v_sub_f32_e32 v34, v2, v3
	v_pk_mul_f32 v[2:3], v[130:131], v[86:87] op_sel:[0,1] op_sel_hi:[1,0]
	v_mul_u32_u24_e32 v64, 0xc0, v170
	v_add_f32_e32 v35, v2, v3
	v_pk_mul_f32 v[2:3], v[132:133], v[88:89]
	v_mul_f32_e32 v18, 0x3c553b94, v18
	v_sub_f32_e32 v36, v2, v3
	v_pk_mul_f32 v[2:3], v[132:133], v[88:89] op_sel:[0,1] op_sel_hi:[1,0]
	v_mul_f32_e32 v19, 0x3c553b94, v19
	v_add_f32_e32 v37, v2, v3
	v_pk_mul_f32 v[2:3], v[126:127], v[90:91]
	v_mov_b32_e32 v138, 0
	v_sub_f32_e32 v50, v2, v3
	v_pk_mul_f32 v[2:3], v[126:127], v[90:91] op_sel:[0,1] op_sel_hi:[1,0]
	v_cvt_pk_fp8_f32 v138, v18, v19
	v_add_f32_e32 v51, v2, v3
	v_pk_mul_f32 v[2:3], v[128:129], v[92:93]
	v_mul_f32_e32 v18, 0x3c553b94, v20
	v_sub_f32_e32 v52, v2, v3
	v_pk_mul_f32 v[2:3], v[128:129], v[92:93] op_sel:[0,1] op_sel_hi:[1,0]
	v_mul_f32_e32 v19, 0x3c553b94, v21
	v_add_f32_e32 v53, v2, v3
	v_pk_mul_f32 v[2:3], v[122:123], v[94:95]
	v_cvt_pk_fp8_f32 v138, v18, v19 op_sel:[0,0,1]
	v_sub_f32_e32 v54, v2, v3
	v_pk_mul_f32 v[2:3], v[122:123], v[94:95] op_sel:[0,1] op_sel_hi:[1,0]
	v_mov_b32_e32 v155, 0
	v_add_f32_e32 v55, v2, v3
	v_pk_mul_f32 v[2:3], v[124:125], v[96:97]
	v_mov_b32_e32 v159, 0
	v_sub_f32_e32 v56, v2, v3
	v_pk_mul_f32 v[2:3], v[124:125], v[96:97] op_sel:[0,1] op_sel_hi:[1,0]
	v_or_b32_e32 v100, 4, v156
	v_add_f32_e32 v57, v2, v3
	v_pk_mul_f32 v[2:3], v[118:119], v[66:67]
	v_or_b32_e32 v101, 5, v156
	v_sub_f32_e32 v6, v2, v3
	v_pk_mul_f32 v[2:3], v[118:119], v[66:67] op_sel:[0,1] op_sel_hi:[1,0]
; __device__ __forceinline__ void qkt(f32x16& p0, f32x16& p1, const char* Ks, const v8i* qr, int r32, int hi, const f32x16& nm16) {
; #pragma unroll
;   for (int s = 0; s < 3; ++s) { const int c0 = 4 * s + 2 * hi;
;     const v8i a0 = __builtin_shufflevector(*reinterpret_cast<const v4i*>(Ks + k8_off(r32, c0)), *reinterpret_cast<const v4i*>(Ks + k8_off(r32, c0 + 1)), 0, 1, 2, 3, 4, 5, 6, 7);
;     const v8i a1 = __builtin_shufflevector(*reinterpret_cast<const v4i*>(Ks + 32 * DQK + k8_off(r32, c0)), *reinterpret_cast<const v4i*>(Ks + 32 * DQK + k8_off(r32, c0 + 1)), 0, 1, 2, 3, 4, 5, 6, 7);
;     p0 = __builtin_amdgcn_mfma_scale_f32_32x32x64_f8f6f4(a0, qr[s], s == 0 ? nm16 : p0, 0, 0, 0, 0, 0, 0);
;     p1 = __builtin_amdgcn_mfma_scale_f32_32x32x64_f8f6f4(a1, qr[s], s == 0 ? nm16 : p1, 0, 0, 0, 0, 0, 0); }
; }
; __device__ __forceinline__ void attn_unit(const unsigned char* __restrict__ CQt, const unsigned char* __restrict__ Wh, const f32x2* __restrict__ cst, const unsigned char* __restrict__ Kh, const unsigned char* __restrict__ Vh, bf16* __restrict__ Ob, char* lds) {
;     ...
;       if (s3 == 2) {
; #pragma unroll
;         for (int r = 0; r < 16; r += 2) { const f32x2 c0 = cc[r >> 1], c1 = cc[8 + (r >> 1)];
;           const float x0 = a0[r], y0 = a0[r + 1], x1 = a1[r], y1 = a1[r + 1];
;           a0[r] = x0 * c0.x - y0 * c0.y; a0[r + 1] = y0 * c0.x + x0 * c0.y; a1[r] = x1 * c1.x - y1 * c1.y; a1[r + 1] = y1 * c1.x + x1 * c1.y; } }
; #pragma unroll
;       for (int q = 0; q < 4; ++q) { int u0 = 0, u1 = 0;
;         u0 = __builtin_amdgcn_cvt_pk_fp8_f32(a0[4 * q] * QS, a0[4 * q + 1] * QS, u0, false); u0 = __builtin_amdgcn_cvt_pk_fp8_f32(a0[4 * q + 2] * QS, a0[4 * q + 3] * QS, u0, true);
;         u1 = __builtin_amdgcn_cvt_pk_fp8_f32(a1[4 * q] * QS, a1[4 * q + 1] * QS, u1, false); u1 = __builtin_amdgcn_cvt_pk_fp8_f32(a1[4 * q + 2] * QS, a1[4 * q + 3] * QS, u1, true);
;         qr[s3][q] = u0; qr[s3][4 + q] = u1; }
;     }
;     asm volatile("s_waitcnt lgkmcnt(0)" ::: "memory"); __builtin_amdgcn_s_barrier(); asm volatile("" ::: "memory");
;   }
;   ADMA(1, 1);
;   qkt(pA0, pA1, lds + KS(0), qr, r32, hi, nm16); partialSM<true>(pA0, pA1, m_reg, nm16, alA);
	v_mul_f32_e32 v6, 0x3c553b94, v6
	v_add_f32_e32 v7, v2, v3
	v_pk_mul_f32 v[2:3], v[120:121], v[68:69]
	v_mul_f32_e32 v7, 0x3c553b94, v7
	v_sub_f32_e32 v8, v2, v3
	v_pk_mul_f32 v[2:3], v[120:121], v[68:69] op_sel:[0,1] op_sel_hi:[1,0]
	v_cvt_pk_fp8_f32 v154, v6, v7
	v_add_f32_e32 v9, v2, v3
	v_pk_mul_f32 v[2:3], v[114:115], v[70:71]
	v_bitop3_b32 v6, v99, v65, 3 bitop3:0x78
	v_sub_f32_e32 v12, v2, v3
	v_pk_mul_f32 v[2:3], v[114:115], v[70:71] op_sel:[0,1] op_sel_hi:[1,0]
	v_lshlrev_b32_e32 v203, 4, v6
	v_add_f32_e32 v13, v2, v3
	v_pk_mul_f32 v[2:3], v[116:117], v[72:73]
	v_or_b32_e32 v6, v203, v64
	v_sub_f32_e32 v38, v2, v3
	v_pk_mul_f32 v[2:3], v[116:117], v[72:73] op_sel:[0,1] op_sel_hi:[1,0]
	v_add_u32_e32 v197, 0, v6
	v_add_f32_e32 v39, v2, v3
	v_pk_mul_f32 v[2:3], v[110:111], v[74:75]
	v_mul_f32_e32 v42, 0x3c553b94, v12
	v_sub_f32_e32 v40, v2, v3
	v_pk_mul_f32 v[2:3], v[110:111], v[74:75] op_sel:[0,1] op_sel_hi:[1,0]
	v_mul_f32_e32 v43, 0x3c553b94, v13
	v_add_f32_e32 v41, v2, v3
	v_pk_mul_f32 v[2:3], v[112:113], v[76:77]
	v_cvt_pk_fp8_f32 v155, v42, v43
	v_sub_f32_e32 v58, v2, v3
	v_pk_mul_f32 v[2:3], v[112:113], v[76:77] op_sel:[0,1] op_sel_hi:[1,0]
	v_or_b32_e32 v102, 8, v156
	v_add_f32_e32 v59, v2, v3
	v_pk_mul_f32 v[2:3], v[106:107], v[78:79]
	v_or_b32_e32 v103, 9, v156
	v_sub_f32_e32 v60, v2, v3
	v_pk_mul_f32 v[2:3], v[106:107], v[78:79] op_sel:[0,1] op_sel_hi:[1,0]
	v_mul_f32_e32 v10, 0x3c553b94, v10
	v_add_f32_e32 v61, v2, v3
	v_pk_mul_f32 v[2:3], v[108:109], v[80:81]
	v_mul_f32_e32 v11, 0x3c553b94, v11
	v_sub_f32_e32 v62, v2, v3
	v_pk_mul_f32 v[2:3], v[108:109], v[80:81] op_sel:[0,1] op_sel_hi:[1,0]
	v_mul_f32_e32 v50, 0x3c553b94, v50
	v_add_f32_e32 v63, v2, v3
	v_mul_f32_e32 v2, 0x3c553b94, v8
	v_mul_f32_e32 v3, 0x3c553b94, v9
	v_cvt_pk_fp8_f32 v154, v2, v3 op_sel:[0,0,1]
	v_mul_f32_e32 v2, 0x3c553b94, v4
	v_mul_f32_e32 v3, 0x3c553b94, v5
	v_cvt_pk_fp8_f32 v158, v2, v3
	v_lshl_add_u64 v[2:3], v[168:169], 0, 64
	global_load_lds_dwordx4 v[2:3], off
	v_bitop3_b32 v2, v156, v65, 3 bitop3:0x78
	v_lshlrev_b32_e32 v202, 4, v2
	v_or_b32_e32 v2, v202, v64
	v_add_u32_e32 v196, 0, v2
	ds_read_b128 v[2:5], v196 offset:8192
	ds_read_b128 v[6:9], v197 offset:8192
	s_waitcnt lgkmcnt(0)
	v_mfma_f32_32x32x64_f8f6f4 v[18:33], v[2:9], v[138:145], 0
	v_mul_f32_e32 v4, 0x3c553b94, v34
	v_mul_f32_e32 v5, 0x3c553b94, v35
	v_cvt_pk_fp8_f32 v159, v4, v5
	v_mul_f32_e32 v2, 0x3c553b94, v38
	v_mul_f32_e32 v3, 0x3c553b94, v39
	v_cvt_pk_fp8_f32 v155, v2, v3 op_sel:[0,0,1]
	v_mul_f32_e32 v2, 0x3c553b94, v36
	v_mul_f32_e32 v3, 0x3c553b94, v37
	v_cvt_pk_fp8_f32 v159, v2, v3 op_sel:[0,0,1]
	v_mul_f32_e32 v2, 0x3c553b94, v40
	v_mul_f32_e32 v3, 0x3c553b94, v41
	v_mov_b32_e32 v156, 0
	v_cvt_pk_fp8_f32 v156, v2, v3
	v_bitop3_b32 v2, v100, v65, 3 bitop3:0x78
	v_bitop3_b32 v6, v101, v65, 3 bitop3:0x78
	v_lshl_add_u32 v2, v2, 4, v64
	v_lshl_add_u32 v6, v6, 4, v64
	v_cvt_pk_fp8_f32 v158, v10, v11 op_sel:[0,0,1]
	ds_read_b128 v[10:13], v196 offset:14336
	ds_read_b128 v[14:17], v197 offset:14336
	v_add_u32_e32 v198, 0, v2
	v_add_u32_e32 v199, 0, v6
	ds_read_b128 v[2:5], v198 offset:8192
	ds_read_b128 v[6:9], v199 offset:8192
	s_waitcnt lgkmcnt(0)
	v_mfma_f32_32x32x64_f8f6f4 v[34:49], v[10:17], v[138:145], 0
	v_mul_f32_e32 v51, 0x3c553b94, v51
	v_mov_b32_e32 v160, 0
	v_cvt_pk_fp8_f32 v160, v50, v51
	v_mov_b32_e32 v157, 0
	v_mul_f32_e32 v10, 0x3c553b94, v58
	v_mul_f32_e32 v11, 0x3c553b94, v59
	v_mov_b32_e32 v161, 0
	v_cvt_pk_fp8_f32 v156, v10, v11 op_sel:[0,0,1]
	ds_read_b128 v[10:13], v198 offset:14336
	ds_read_b128 v[14:17], v199 offset:14336
	s_mov_b32 s8, s9
	s_mov_b32 s10, s9
	s_mov_b32 s11, s9
	s_mov_b32 s12, s9
	s_mov_b32 s13, s9
	s_mov_b32 s14, s9
	v_mfma_f32_32x32x64_f8f6f4 v[18:33], v[2:9], v[146:153], v[18:33]
	v_mul_f32_e32 v4, 0x3c553b94, v60
	v_mul_f32_e32 v5, 0x3c553b94, v61
	v_cvt_pk_fp8_f32 v157, v4, v5
	v_mul_f32_e32 v2, 0x3c553b94, v52
	v_mul_f32_e32 v3, 0x3c553b94, v53
	v_cvt_pk_fp8_f32 v160, v2, v3 op_sel:[0,0,1]
	v_mul_f32_e32 v2, 0x3c553b94, v62
	v_mul_f32_e32 v3, 0x3c553b94, v63
	v_cvt_pk_fp8_f32 v157, v2, v3 op_sel:[0,0,1]
	v_mul_f32_e32 v2, 0x3c553b94, v54
	v_mul_f32_e32 v3, 0x3c553b94, v55
	v_cvt_pk_fp8_f32 v161, v2, v3
	v_bitop3_b32 v2, v102, v65, 3 bitop3:0x78
	v_bitop3_b32 v6, v103, v65, 3 bitop3:0x78
	v_lshl_add_u32 v2, v2, 4, v64
	v_lshl_add_u32 v6, v6, 4, v64
	v_add_u32_e32 v200, 0, v2
	v_add_u32_e32 v201, 0, v6
	ds_read_b128 v[2:5], v200 offset:8192
	ds_read_b128 v[6:9], v201 offset:8192
	s_waitcnt lgkmcnt(0)
	v_mfma_f32_32x32x64_f8f6f4 v[34:49], v[10:17], v[146:153], v[34:49]
	v_mul_f32_e32 v10, 0x3c553b94, v56
	v_mul_f32_e32 v11, 0x3c553b94, v57
	v_cvt_pk_fp8_f32 v161, v10, v11 op_sel:[0,0,1]
	ds_read_b128 v[50:53], v200 offset:14336
	ds_read_b128 v[54:57], v201 offset:14336
	s_mov_b32 s15, s9
	s_mov_b32 s16, s9
	s_mov_b32 s17, s9
	s_mov_b32 s18, s9
	s_mov_b32 s19, s9
	s_mov_b32 s20, s9
	s_mov_b32 s21, s9
	s_mov_b32 s22, s9
	s_mov_b32 s23, s9
	v_mov_b32_e32 v66, 0
	v_mov_b32_e32 v67, 0
	v_mfma_f32_32x32x64_f8f6f4 v[18:33], v[2:9], v[154:161], v[18:33]
	v_mov_b64_e32 v[2:3], s[8:9]
	v_mov_b64_e32 v[4:5], s[10:11]
	v_mov_b64_e32 v[6:7], s[12:13]
	v_mov_b64_e32 v[8:9], s[14:15]
	v_mov_b64_e32 v[10:11], s[16:17]
	v_mov_b64_e32 v[12:13], s[18:19]
	v_mov_b64_e32 v[14:15], s[20:21]
	v_mov_b64_e32 v[16:17], s[22:23]
	s_lshl_b32 s8, s33, 10
	s_and_b32 s8, s8, 0xffff0000
	v_mov_b32_e32 v68, 0
	v_mov_b32_e32 v69, 0
	v_mov_b32_e32 v70, 0
	v_mov_b32_e32 v71, 0
	v_mov_b32_e32 v72, 0
	s_waitcnt lgkmcnt(0)
; template <bool FIRST>
; __device__ __forceinline__ void partialSM(f32x16& p0, f32x16& p1, float& m_reg, f32x16& nm16, float& alpha) {
;   float pmax = p0[0];
; #pragma unroll
;   for (int r = 1; r < 16; ++r) pmax = fmaxf(pmax, p0[r]);
; #pragma unroll
;   for (int r = 0; r < 16; ++r) pmax = fmaxf(pmax, p1[r]);
;   { auto rr = __builtin_amdgcn_permlane32_swap(__float_as_uint(pmax), __float_as_uint(pmax), false, false);
;     pmax = fmaxf(__uint_as_float(rr[0]), __uint_as_float(rr[1])); }
;   if (!FIRST && __builtin_expect(__all(pmax <= THR2), 1)) { alpha = 1.f; }
;   else { const float d = FIRST ? pmax : fmaxf(pmax, 0.f);
;     alpha = FIRST ? 1.f : __builtin_amdgcn_exp2f(-d); m_reg += d;
;     const float nm = -m_reg;
; #pragma unroll
;     for (int r = 0; r < 16; ++r) { p0[r] -= d; p1[r] -= d; float t = nm16[r]; asm volatile("v_mov_b32 %0, %1" : "+v"(t) : "v"(nm)); nm16[r] = t; } }
; #pragma unroll
;   for (int r = 0; r < 16; ++r) p0[r] = __builtin_amdgcn_exp2f(p0[r]);
; }
	v_mfma_f32_32x32x64_f8f6f4 v[34:49], v[50:57], v[154:161], v[34:49]
	s_nop 2
	v_max_f32_e32 v50, v19, v19
	v_max_f32_e32 v51, v18, v18
	v_max_f32_e32 v50, v51, v50
	v_max3_f32 v50, v50, v20, v21
	v_max3_f32 v50, v50, v22, v23
	v_max3_f32 v50, v50, v24, v25
	v_max3_f32 v50, v50, v26, v27
	v_max3_f32 v50, v50, v28, v29
	v_max3_f32 v50, v50, v30, v31
	v_max3_f32 v50, v50, v32, v33
	v_mov_b32_e32 v73, 0
	v_mov_b32_e32 v74, 0
	v_mov_b32_e32 v75, 0
	v_mov_b32_e32 v76, 0
	v_mov_b32_e32 v77, 0
	s_nop 1
	v_max3_f32 v50, v50, v34, v35
	v_max3_f32 v50, v50, v36, v37
	v_max3_f32 v50, v50, v38, v39
	v_max3_f32 v50, v50, v40, v41
	v_max3_f32 v50, v50, v42, v43
	v_max3_f32 v50, v50, v44, v45
	v_max3_f32 v50, v50, v46, v47
	v_max3_f32 v50, v50, v48, v49
	v_mov_b32_e32 v51, v50
	s_nop 1
	v_permlane32_swap_b32_e32 v50, v51
	v_max_f32_e32 v51, v51, v51
	v_max_f32_e32 v50, v50, v50
	v_max_f32_e32 v50, v50, v51
	v_sub_f32_e32 v18, v18, v50
	v_add_f32_e32 v195, 0, v50
	v_sub_f32_e32 v19, v19, v50
	v_sub_f32_e32 v20, v20, v50
	v_sub_f32_e32 v21, v21, v50
	v_sub_f32_e32 v22, v22, v50
	v_sub_f32_e32 v23, v23, v50
	v_sub_f32_e32 v24, v24, v50
	v_sub_f32_e32 v25, v25, v50
	v_sub_f32_e32 v26, v26, v50
	v_sub_f32_e32 v27, v27, v50
	v_sub_f32_e32 v28, v28, v50
	v_sub_f32_e32 v29, v29, v50
	v_sub_f32_e32 v30, v30, v50
	v_mov_b32_e32 v78, 0
	v_sub_f32_e32 v31, v31, v50
	v_mov_b32_e32 v79, 0
	v_sub_f32_e32 v32, v32, v50
	v_mov_b32_e32 v80, 0
	v_sub_f32_e32 v33, v33, v50
	v_mov_b32_e32 v81, 0
	v_exp_f32_e32 v235, v18
	v_lshl_or_b32 v18, v171, 10, s8
	s_lshl_b32 s2, s2, 2
	v_xor_b32_e32 v51, 0x80000000, v195
	v_mov_b32 v66, v51
	v_mov_b32 v67, v51
	v_mov_b32 v68, v51
	v_mov_b32 v69, v51
	v_mov_b32 v70, v51
	v_mov_b32 v71, v51
	v_mov_b32 v72, v51
	v_mov_b32 v73, v51
	v_mov_b32 v74, v51
	v_mov_b32 v75, v51
	v_mov_b32 v76, v51
	v_mov_b32 v77, v51
	v_mov_b32 v78, v51
	v_mov_b32 v79, v51
	v_mov_b32 v80, v51
	v_mov_b32 v81, v51
	v_exp_f32_e32 v236, v19
	v_exp_f32_e32 v233, v20
	v_exp_f32_e32 v234, v21
	v_exp_f32_e32 v231, v22
	v_exp_f32_e32 v232, v23
	v_exp_f32_e32 v229, v24
	v_exp_f32_e32 v230, v25
	v_exp_f32_e32 v227, v26
	v_exp_f32_e32 v228, v27
	v_exp_f32_e32 v225, v28
	v_exp_f32_e32 v226, v29
	v_exp_f32_e32 v223, v30
	v_exp_f32_e32 v224, v31
	v_exp_f32_e32 v221, v32
	v_exp_f32_e32 v222, v33
	s_waitcnt vmcnt(0)
	v_and_or_b32 v18, v18, s84, v172
	s_add_i32 s93, s2, 0
	s_barrier
	v_ashrrev_i32_e32 v19, 31, v18
	v_lshlrev_b32_e32 v98, 4, v190
	v_mov_b32_e32 v162, 0
	v_sub_f32_e32 v97, v49, v50
	v_sub_f32_e32 v96, v48, v50
	v_sub_f32_e32 v95, v47, v50
	v_sub_f32_e32 v94, v46, v50
	v_sub_f32_e32 v93, v45, v50
	v_sub_f32_e32 v92, v44, v50
	v_sub_f32_e32 v91, v43, v50
	v_sub_f32_e32 v90, v42, v50
	v_sub_f32_e32 v89, v41, v50
	v_sub_f32_e32 v88, v40, v50
	v_sub_f32_e32 v87, v39, v50
	v_sub_f32_e32 v86, v38, v50
	v_sub_f32_e32 v85, v37, v50
	v_sub_f32_e32 v84, v36, v50
	v_sub_f32_e32 v83, v35, v50
	v_sub_f32_e32 v82, v34, v50
	v_lshl_add_u32 v204, v170, 6, 0
	v_cmp_gt_u32_e64 s[2:3], 32, v171
	v_lshl_add_u32 v192, v170, 2, s93
	v_lshl_add_u64 v[170:171], s[66:67], 0, v[18:19]
	v_mov_b64_e32 v[64:65], v[16:17]
	v_mov_b64_e32 v[48:49], v[16:17]
	v_mov_b64_e32 v[32:33], v[16:17]
	v_add_u32_e32 v191, s93, v98
	v_lshl_add_u64 v[172:173], v[166:167], 0, s[4:5]
	v_lshl_add_u64 v[174:175], s[4:5], 0, v[164:165]
	s_add_u32 s24, s0, 0x6000
	s_addc_u32 s25, s1, 0
	s_add_u32 s26, s6, 0x4e000040
	s_addc_u32 s27, s7, 0
	s_and_b32 s94, s64, 1
	s_cmp_eq_u32 s94, 0
	s_cbranch_scc0 .Lstg_pre_l1
	s_mov_b32 m0, s90
	s_nop 0
	global_load_lds_dwordx4 v164, s[24:25]
	s_mov_b32 m0, s88
	s_nop 0
	global_load_lds_dwordx4 v170, s[26:27]
	s_add_u32 s24, s24, 0x3000
	s_addc_u32 s25, s25, 0
	s_add_u32 s26, s26, 64
	s_addc_u32 s27, s27, 0
.Lstg_pre_l1:
	v_mov_b32_e32 v205, 1.0
	s_mov_b32 s8, -5
	v_mov_b64_e32 v[62:63], v[14:15]
	v_mov_b64_e32 v[60:61], v[12:13]
	v_mov_b64_e32 v[58:59], v[10:11]
	v_mov_b64_e32 v[56:57], v[8:9]
	v_mov_b64_e32 v[54:55], v[6:7]
	v_mov_b64_e32 v[52:53], v[4:5]
	v_mov_b64_e32 v[50:51], v[2:3]
	v_mov_b64_e32 v[46:47], v[14:15]
	v_mov_b64_e32 v[44:45], v[12:13]
	v_mov_b64_e32 v[42:43], v[10:11]
	v_mov_b64_e32 v[40:41], v[8:9]
	v_mov_b64_e32 v[38:39], v[6:7]
	v_mov_b64_e32 v[36:37], v[4:5]
	v_mov_b64_e32 v[34:35], v[2:3]
	v_mov_b64_e32 v[30:31], v[14:15]
	v_mov_b64_e32 v[28:29], v[12:13]
	v_mov_b64_e32 v[26:27], v[10:11]
	v_mov_b64_e32 v[24:25], v[8:9]
	v_mov_b64_e32 v[22:23], v[6:7]
	v_mov_b64_e32 v[20:21], v[4:5]
	v_mov_b64_e32 v[18:19], v[2:3]
	v_mov_b32_e32 v130, 0
	v_mov_b32_e32 v131, v162
	v_mov_b32_e32 v132, v162
	v_mov_b32_e32 v133, v162
	v_mov_b32_e32 v134, v162
	v_mov_b32_e32 v135, v162
	v_mov_b32_e32 v136, v162
	v_mov_b32_e32 v137, v162

; __device__ __forceinline__ void finishSM(f32x16& p0, f32x16& p1, float alpha, float& l_reg, v8i& pa) {
; #pragma unroll
;   for (int r = 0; r < 16; ++r) p1[r] = __builtin_amdgcn_exp2f(p1[r]);
;   float ps = 0;
; #pragma unroll
;   for (int r = 0; r < 16; ++r) ps += p0[r];
; #pragma unroll
;   for (int r = 0; r < 16; ++r) ps += p1[r];
;   { auto rr = __builtin_amdgcn_permlane32_swap(__float_as_uint(ps), __float_as_uint(ps), false, false);
;     ps = __uint_as_float(rr[0]) + __uint_as_float(rr[1]); }
;   l_reg = l_reg * alpha + ps;
; #pragma unroll
;   for (int q = 0; q < 4; ++q) { int w0 = pa[q], w1 = pa[4 + q];
;     w0 = __builtin_amdgcn_cvt_pk_fp8_f32(p0[4 * q], p0[4 * q + 1], w0, false); w0 = __builtin_amdgcn_cvt_pk_fp8_f32(p0[4 * q + 2], p0[4 * q + 3], w0, true);
;     w1 = __builtin_amdgcn_cvt_pk_fp8_f32(p1[4 * q], p1[4 * q + 1], w1, false); w1 = __builtin_amdgcn_cvt_pk_fp8_f32(p1[4 * q + 2], p1[4 * q + 3], w1, true);
;     pa[q] = w0; pa[4 + q] = w1; }
; }
; __device__ __forceinline__ void qkt(f32x16& p0, f32x16& p1, const char* Ks, const v8i* qr, int r32, int hi, const f32x16& nm16) {
; #pragma unroll
;   for (int s = 0; s < 3; ++s) { const int c0 = 4 * s + 2 * hi;
;     const v8i a0 = __builtin_shufflevector(*reinterpret_cast<const v4i*>(Ks + k8_off(r32, c0)), *reinterpret_cast<const v4i*>(Ks + k8_off(r32, c0 + 1)), 0, 1, 2, 3, 4, 5, 6, 7);
;     const v8i a1 = __builtin_shufflevector(*reinterpret_cast<const v4i*>(Ks + 32 * DQK + k8_off(r32, c0)), *reinterpret_cast<const v4i*>(Ks + 32 * DQK + k8_off(r32, c0 + 1)), 0, 1, 2, 3, 4, 5, 6, 7);
;     p0 = __builtin_amdgcn_mfma_scale_f32_32x32x64_f8f6f4(a0, qr[s], s == 0 ? nm16 : p0, 0, 0, 0, 0, 0, 0);
;     p1 = __builtin_amdgcn_mfma_scale_f32_32x32x64_f8f6f4(a1, qr[s], s == 0 ? nm16 : p1, 0, 0, 0, 0, 0, 0); }
; }
; __device__ __forceinline__ void pv_d0(f32x16* o, const char* Vs, v8i pa, int r32, int hi) {
; #pragma unroll
;   for (int d0 = 0; d0 < 4; ++d0) { const int row = 32 * d0 + r32, x = (row >> 2) & 3;
;     const v8i vb = __builtin_shufflevector(*reinterpret_cast<const v4i*>(Vs + row * 64 + (((2 * hi) ^ x) << 4)), *reinterpret_cast<const v4i*>(Vs + row * 64 + (((2 * hi + 1) ^ x) << 4)), 0, 1, 2, 3, 4, 5, 6, 7);
;     o[d0] = __builtin_amdgcn_mfma_scale_f32_32x32x64_f8f6f4(pa, vb, o[d0], 0, 0, 0, 0, 0, 0); }
; }
.Lstg_end4_l1:
	v_exp_f32_e32 v176, v114
	v_exp_f32_e32 v177, v115
	v_exp_f32_e32 v178, v116
	v_exp_f32_e32 v179, v117
	v_exp_f32_e32 v180, v118
	v_exp_f32_e32 v181, v119
	v_exp_f32_e32 v182, v120
	v_exp_f32_e32 v183, v121
	v_exp_f32_e32 v184, v122
	v_exp_f32_e32 v185, v123
	v_exp_f32_e32 v221, v124
	v_exp_f32_e32 v238, v125
	v_exp_f32_e32 v239, v126
	v_exp_f32_e32 v240, v127
	v_exp_f32_e32 v241, v128
	v_exp_f32_e32 v242, v129
	ds_read_b128 v[82:85], v196 offset:8192
	ds_read_b128 v[86:89], v197 offset:8192
	ds_read_b128 v[222:225], v196 offset:14336
	ds_read_b128 v[226:229], v197 offset:14336
	v_exp_f32_e32 v100, v100
	v_exp_f32_e32 v101, v101
	s_waitcnt lgkmcnt(0)
	v_mfma_f32_32x32x64_f8f6f4 v[114:129], v[82:89], v[138:145], v[66:81]
	v_exp_f32_e32 v102, v102
	v_exp_f32_e32 v103, v103
	v_exp_f32_e32 v104, v104
	v_exp_f32_e32 v105, v105
	v_exp_f32_e32 v106, v106
	v_exp_f32_e32 v107, v107
	v_exp_f32_e32 v108, v108
	v_exp_f32_e32 v110, v110
	v_exp_f32_e32 v111, v111
	v_exp_f32_e32 v109, v109
	v_exp_f32_e32 v112, v112
	v_exp_f32_e32 v113, v113
	v_cvt_pk_fp8_f32 v130, v176, v177
	v_cvt_pk_fp8_f32 v131, v180, v181
	v_cvt_pk_fp8_f32 v135, v102, v103
	v_mfma_f32_32x32x64_f8f6f4 v[82:97], v[222:229], v[138:145], v[66:81]
	ds_read_b128 v[222:225], v198 offset:8192
	ds_read_b128 v[226:229], v199 offset:8192
	ds_read_b128 v[230:233], v198 offset:14336
	ds_read_b128 v[234:237], v199 offset:14336
	v_cvt_pk_fp8_f32 v132, v184, v185
	v_cvt_pk_fp8_f32 v136, v106, v107
	v_cvt_pk_fp8_f32 v133, v239, v240
	v_cvt_pk_fp8_f32 v137, v110, v111
	v_cvt_pk_fp8_f32 v130, v178, v179 op_sel:[0,0,1]
	v_cvt_pk_fp8_f32 v131, v182, v183 op_sel:[0,0,1]
	v_cvt_pk_fp8_f32 v135, v104, v105 op_sel:[0,0,1]
	v_cvt_pk_fp8_f32 v132, v221, v238 op_sel:[0,0,1]
	v_cvt_pk_fp8_f32 v136, v108, v109 op_sel:[0,0,1]
	v_cvt_pk_fp8_f32 v133, v241, v242 op_sel:[0,0,1]
	v_cvt_pk_fp8_f32 v137, v112, v113 op_sel:[0,0,1]
	s_waitcnt lgkmcnt(0)
	v_mfma_f32_32x32x64_f8f6f4 v[114:129], v[222:229], v[146:153], v[114:129]
	v_mfma_f32_32x32x64_f8f6f4 v[82:97], v[230:237], v[146:153], v[82:97]
	ds_read_b128 v[222:225], v200 offset:8192
	ds_read_b128 v[226:229], v201 offset:8192
	ds_read_b128 v[230:233], v200 offset:14336
	ds_read_b128 v[234:237], v201 offset:14336
	s_waitcnt lgkmcnt(0)
	v_mfma_f32_32x32x64_f8f6f4 v[114:129], v[222:229], v[154:161], v[114:129]
	v_exp_f32_e32 v222, v98
	v_add_f32_e32 v98, 0, v176
	v_add_f32_e32 v98, v177, v98
	v_add_f32_e32 v98, v178, v98
	v_add_f32_e32 v98, v179, v98
	v_add_f32_e32 v98, v180, v98
	v_add_f32_e32 v98, v181, v98
	v_add_f32_e32 v98, v182, v98
	v_add_f32_e32 v98, v183, v98
	v_add_f32_e32 v98, v184, v98
	v_add_f32_e32 v98, v185, v98
	v_add_f32_e32 v98, v221, v98
	v_add_f32_e32 v98, v238, v98
	v_add_f32_e32 v98, v239, v98
	v_exp_f32_e32 v223, v99
	v_add_f32_e32 v98, v240, v98
	v_add_f32_e32 v98, v241, v98
	v_add_f32_e32 v98, v242, v98
	v_add_f32_e32 v98, v222, v98
	v_add_f32_e32 v98, v223, v98
	v_mfma_f32_32x32x64_f8f6f4 v[82:97], v[230:237], v[154:161], v[82:97]
	v_add_f32_e32 v98, v100, v98
	v_add_f32_e32 v98, v101, v98
	v_add_f32_e32 v98, v102, v98
	v_add_f32_e32 v98, v103, v98
	v_add_f32_e32 v98, v104, v98
	v_add_f32_e32 v98, v105, v98
	v_add_f32_e32 v98, v106, v98
	v_add_f32_e32 v98, v107, v98
	v_add_f32_e32 v98, v108, v98
	v_cvt_pk_fp8_f32 v134, v222, v223
	v_add_f32_e32 v98, v109, v98
	v_add_f32_e32 v98, v110, v98
	v_add_f32_e32 v98, v111, v98
	v_add_f32_e32 v98, v112, v98
	v_cvt_pk_fp8_f32 v134, v100, v101 op_sel:[0,0,1]
	v_add_f32_e32 v98, v113, v98
	v_mov_b32_e32 v99, v98
	s_nop 1
	v_permlane32_swap_b32_e32 v98, v99
	s_cmp_eq_u32 s94, 0
	s_cbranch_scc0 .Lstg_mid5_l1
	s_waitcnt vmcnt(0)
	s_barrier
	s_cmp_lt_i32 s8, 49
	s_cbranch_scc0 .Lstg_mid5_l1
	s_mov_b32 m0, s90
	s_nop 0
	global_load_lds_dwordx4 v164, s[24:25]
	s_mov_b32 m0, s88
	s_nop 0
	global_load_lds_dwordx4 v170, s[26:27]
	s_add_u32 s24, s24, 0x3000
	s_addc_u32 s25, s25, 0
	s_add_u32 s26, s26, 64
	s_addc_u32 s27, s27, 0

; #define ASTEP_B(jt, bp, bc, bn) ASTEP(pB0, pB1, alB, pA0, pA1, alA, jt, bp, bc, bn)
; #define ASTEP_A(jt, bp, bc, bn) ASTEP(pA0, pA1, alA, pB0, pB1, alB, jt, bp, bc, bn)
; __device__ __forceinline__ void finishSM(f32x16& p0, f32x16& p1, float alpha, float& l_reg, v8i& pa) {
; #pragma unroll
;   for (int r = 0; r < 16; ++r) p1[r] = __builtin_amdgcn_exp2f(p1[r]);
;   float ps = 0;
; #pragma unroll
;   for (int r = 0; r < 16; ++r) ps += p0[r];
; #pragma unroll
;   for (int r = 0; r < 16; ++r) ps += p1[r];
;   { auto rr = __builtin_amdgcn_permlane32_swap(__float_as_uint(ps), __float_as_uint(ps), false, false);
;     ps = __uint_as_float(rr[0]) + __uint_as_float(rr[1]); }
;   l_reg = l_reg * alpha + ps;
; #pragma unroll
;   for (int q = 0; q < 4; ++q) { int w0 = pa[q], w1 = pa[4 + q];
;     w0 = __builtin_amdgcn_cvt_pk_fp8_f32(p0[4 * q], p0[4 * q + 1], w0, false); w0 = __builtin_amdgcn_cvt_pk_fp8_f32(p0[4 * q + 2], p0[4 * q + 3], w0, true);
;     w1 = __builtin_amdgcn_cvt_pk_fp8_f32(p1[4 * q], p1[4 * q + 1], w1, false); w1 = __builtin_amdgcn_cvt_pk_fp8_f32(p1[4 * q + 2], p1[4 * q + 3], w1, true);
;     pa[q] = w0; pa[4 + q] = w1; }
; }
; __device__ __forceinline__ void attn_unit(const unsigned char* __restrict__ CQt, const unsigned char* __restrict__ Wh, const f32x2* __restrict__ cst, const unsigned char* __restrict__ Kh, const unsigned char* __restrict__ Vh, bf16* __restrict__ Ob, char* lds) {
;     ...
; #pragma nounroll
;   for (int j = 1; j <= 55; j += 6) {
;     ASTEP_B(j, 0, 1, 2); ASTEP_A(j + 1, 1, 2, 0); ASTEP_B(j + 2, 2, 0, 1);
;     ASTEP_A(j + 3, 0, 1, 2); ASTEP_B(j + 4, 1, 2, 0); ASTEP_A(j + 5, 2, 0, 1);
;   }
.Lstg_end5_l1:
	v_fmac_f32_e32 v100, v101, v217
	v_add_f32_e32 v162, v98, v99
	s_add_i32 s8, s8, 6
	v_fmac_f32_e32 v162, v100, v220
	s_cmp_gt_u32 s8, 49
	s_cbranch_scc1 .LBB0_2200
	v_mov_b32_e32 v205, v176
	s_branch .LBB0_2150
